# GELU epilogue uses abs source modifiers with SGPR constants (one VALU fewer per element); otherwise as v28
# speedup vs baseline: 1.0860x; 1.0014x over previous
_Z6gemm_kILi1ELi2ELi2EEvPKDF16_S1_iiiPKfS1_PDF16_PfS4_:
	s_lshr_b32 s37, s2, 3
	s_cmp_lt_u32 s37, 32
	s_cbranch_scc1 Lg1_exit
	s_sub_u32 s37, s37, 32
	s_and_b32 s36, s2, 7
	s_lshr_b32 s38, s37, 2
	s_lshl_b32 s36, s36, 3
	s_add_u32 s22, s36, s38
	s_and_b32 s21, s37, 3
	s_cmp_ge_u32 s22, 63
	s_cbranch_scc1 Lg1_exit
	s_load_dwordx4 s[4:7], s[0:1], 0x0
	s_load_dwordx4 s[8:11], s[0:1], 0x20
	s_load_dwordx4 s[12:15], s[0:1], 0x30
	s_load_dwordx2 s[16:17], s[0:1], 0x40
	v_lshrrev_b32_e32 v20, 6, v0
	v_and_b32_e32 v1, 63, v0
	v_readfirstlane_b32 s20, v20
	v_and_b32_e32 v2, 15, v0
	v_bfe_u32 v3, v0, 4, 2
	v_and_b32_e32 v16, 7, v2
	v_xor_b32_e32 v16, v16, v3
	v_lshlrev_b32_e32 v16, 4, v16
	v_lshl_or_b32 v4, v2, 7, v16
	v_lshrrev_b32_e32 v16, 3, v1
	v_and_b32_e32 v17, 7, v1
	v_xor_b32_e32 v17, v17, v16
	v_lshlrev_b32_e32 v17, 4, v17
	v_lshl_or_b32 v9, v16, 7, v17
	v_add_u32_e32 v10, 0x140000, v9
	s_mul_i32 s23, s22, 10
	s_sub_u32 s24, 625, s23
	s_min_u32 s24, s24, 10
	s_waitcnt lgkmcnt(0)
	s_mul_i32 s36, s20, 0x280000
	s_lshl_b32 s37, s23, 11
	s_add_u32 s36, s36, s37
	s_add_u32 s26, s4, s36
	s_addc_u32 s27, s5, 0
	s_mul_i32 s28, s20, 0x1000
	s_add_u32 s46, s28, 0x14000
	s_mov_b32 s47, s28
	s_mov_b32 s29, 0
	s_lshl_b32 s36, s21, 8
	s_lshl_b32 s37, s20, 6
	s_add_u32 s36, s36, s37
	v_lshlrev_b32_e32 v16, 4, v3
	v_add_u32_e32 v16, s36, v16
	v_lshlrev_b32_e32 v17, 2, v16
	global_load_dwordx4 v[32:35], v17, s[8:9] offset:0
	global_load_dwordx4 v[36:39], v17, s[8:9] offset:16
	global_load_dwordx4 v[40:43], v17, s[8:9] offset:32
	global_load_dwordx4 v[44:47], v17, s[8:9] offset:48
	v_mov_b32_e32 v113, 0x36b49f67
	s_mov_b32 s48, 0x384d0fec
	s_mov_b32 s49, 0x381f6607
	s_mov_b32 s50, 0x3b56cd72
	s_mov_b32 s51, 0x3cad2fe7
	s_mov_b32 s52, 0x3d4c41b4
	v_mov_b32_e32 v114, 0x36b49f67
	v_mov_b32_e32 v115, 0x36b49f67
	v_mov_b32_e32 v116, 0x384d0fec
	v_mov_b32_e32 v117, 0x384d0fec
	v_mov_b32_e32 v118, 0x381f6607
	v_mov_b32_e32 v119, 0x381f6607
	v_mov_b32_e32 v120, 0x3b56cd72
	v_mov_b32_e32 v121, 0x3b56cd72
	v_mov_b32_e32 v122, 0x3cad2fe7
	v_mov_b32_e32 v123, 0x3cad2fe7
	v_mov_b32_e32 v124, 0x3d4c41b4
	v_mov_b32_e32 v125, 0x3d4c41b4
	v_mov_b32_e32 v126, 0x3f800000
	v_mov_b32_e32 v127, 0x3f800000
	v_lshlrev_b32_e32 v18, 5, v3
	v_lshl_or_b32 v14, v2, 7, v18
	s_lshl_b32 s38, s21, 2
	s_add_u32 s38, s38, s20
	s_mul_i32 s38, s38, 0x140000
	s_lshl_b32 s39, s23, 11
	s_add_u32 s38, s38, s39
	s_add_u32 s30, s12, s38
	s_addc_u32 s31, s13, 0
	s_mov_b32 m0, s28
	s_add_u32 s28, s28, 0x4000
	s_cmp_ge_u32 s28, s46
	s_cselect_b32 s28, s47, s28
	global_load_lds_dwordx4 v9, s[26:27]
	global_load_lds_dwordx4 v9, s[26:27] offset:1024
	s_add_u32 m0, m0, 0x800
	s_nop 0
	global_load_lds_dwordx4 v10, s[26:27]
	global_load_lds_dwordx4 v10, s[26:27] offset:1024
	s_add_u32 s26, s26, 0x800
	s_addc_u32 s27, s27, 0
	s_mov_b32 m0, s28
	s_add_u32 s28, s28, 0x4000
	s_cmp_ge_u32 s28, s46
	s_cselect_b32 s28, s47, s28
	global_load_lds_dwordx4 v9, s[26:27]
	global_load_lds_dwordx4 v9, s[26:27] offset:1024
	s_add_u32 m0, m0, 0x800
	s_nop 0
	global_load_lds_dwordx4 v10, s[26:27]
	global_load_lds_dwordx4 v10, s[26:27] offset:1024
	s_add_u32 s26, s26, 0x800
	s_addc_u32 s27, s27, 0
	s_lshl_b32 s36, s21, 2
	s_add_u32 s36, s36, s20
	s_mul_i32 s36, s36, 0x10000
	v_lshlrev_b32_e32 v16, 4, v1
	v_add_u32_e32 v13, s36, v16
	global_load_dwordx4 a[0:3], v13, s[6:7] offset:0
	global_load_dwordx4 a[4:7], v13, s[6:7] offset:1024
	global_load_dwordx4 a[8:11], v13, s[6:7] offset:2048
	global_load_dwordx4 a[12:15], v13, s[6:7] offset:3072
	v_add_u32_e32 v13, 0x1000, v13
	global_load_dwordx4 a[16:19], v13, s[6:7] offset:0
	global_load_dwordx4 a[20:23], v13, s[6:7] offset:1024
	global_load_dwordx4 a[24:27], v13, s[6:7] offset:2048
	global_load_dwordx4 a[28:31], v13, s[6:7] offset:3072
	v_add_u32_e32 v13, 0x1000, v13
	global_load_dwordx4 a[32:35], v13, s[6:7] offset:0
	global_load_dwordx4 a[36:39], v13, s[6:7] offset:1024
	global_load_dwordx4 a[40:43], v13, s[6:7] offset:2048
	global_load_dwordx4 a[44:47], v13, s[6:7] offset:3072
	v_add_u32_e32 v13, 0x1000, v13
	global_load_dwordx4 a[48:51], v13, s[6:7] offset:0
	global_load_dwordx4 a[52:55], v13, s[6:7] offset:1024
	global_load_dwordx4 a[56:59], v13, s[6:7] offset:2048
	global_load_dwordx4 a[60:63], v13, s[6:7] offset:3072
	v_add_u32_e32 v13, 0x1000, v13
	global_load_dwordx4 a[64:67], v13, s[6:7] offset:0
	global_load_dwordx4 a[68:71], v13, s[6:7] offset:1024
	global_load_dwordx4 a[72:75], v13, s[6:7] offset:2048
	global_load_dwordx4 a[76:79], v13, s[6:7] offset:3072
	v_add_u32_e32 v13, 0x1000, v13
	global_load_dwordx4 a[80:83], v13, s[6:7] offset:0
	global_load_dwordx4 a[84:87], v13, s[6:7] offset:1024
	global_load_dwordx4 a[88:91], v13, s[6:7] offset:2048
	global_load_dwordx4 a[92:95], v13, s[6:7] offset:3072
	v_add_u32_e32 v13, 0x1000, v13
	global_load_dwordx4 a[96:99], v13, s[6:7] offset:0
	global_load_dwordx4 a[100:103], v13, s[6:7] offset:1024
	global_load_dwordx4 a[104:107], v13, s[6:7] offset:2048
	global_load_dwordx4 a[108:111], v13, s[6:7] offset:3072
	v_add_u32_e32 v13, 0x1000, v13
	global_load_dwordx4 a[112:115], v13, s[6:7] offset:0
	global_load_dwordx4 a[116:119], v13, s[6:7] offset:1024
	global_load_dwordx4 a[120:123], v13, s[6:7] offset:2048
	global_load_dwordx4 a[124:127], v13, s[6:7] offset:3072
	v_add_u32_e32 v13, 0x1000, v13
	global_load_dwordx4 a[128:131], v13, s[6:7] offset:0
	global_load_dwordx4 a[132:135], v13, s[6:7] offset:1024
	global_load_dwordx4 a[136:139], v13, s[6:7] offset:2048
	global_load_dwordx4 a[140:143], v13, s[6:7] offset:3072
	v_add_u32_e32 v13, 0x1000, v13
	global_load_dwordx4 a[144:147], v13, s[6:7] offset:0
	global_load_dwordx4 a[148:151], v13, s[6:7] offset:1024
	global_load_dwordx4 a[152:155], v13, s[6:7] offset:2048
	global_load_dwordx4 a[156:159], v13, s[6:7] offset:3072
	v_add_u32_e32 v13, 0x1000, v13
	global_load_dwordx4 a[160:163], v13, s[6:7] offset:0
	global_load_dwordx4 a[164:167], v13, s[6:7] offset:1024
	global_load_dwordx4 a[168:171], v13, s[6:7] offset:2048
	global_load_dwordx4 a[172:175], v13, s[6:7] offset:3072
	v_add_u32_e32 v13, 0x1000, v13
	global_load_dwordx4 a[176:179], v13, s[6:7] offset:0
	global_load_dwordx4 a[180:183], v13, s[6:7] offset:1024
	global_load_dwordx4 a[184:187], v13, s[6:7] offset:2048
	global_load_dwordx4 a[188:191], v13, s[6:7] offset:3072
	v_add_u32_e32 v13, 0x1000, v13
	global_load_dwordx4 a[192:195], v13, s[6:7] offset:0
	global_load_dwordx4 a[196:199], v13, s[6:7] offset:1024
	global_load_dwordx4 a[200:203], v13, s[6:7] offset:2048
	global_load_dwordx4 a[204:207], v13, s[6:7] offset:3072
	v_add_u32_e32 v13, 0x1000, v13
	global_load_dwordx4 a[208:211], v13, s[6:7] offset:0
	global_load_dwordx4 a[212:215], v13, s[6:7] offset:1024
	global_load_dwordx4 a[216:219], v13, s[6:7] offset:2048
	global_load_dwordx4 a[220:223], v13, s[6:7] offset:3072
	v_add_u32_e32 v13, 0x1000, v13
	global_load_dwordx4 a[224:227], v13, s[6:7] offset:0
	global_load_dwordx4 a[228:231], v13, s[6:7] offset:1024
	global_load_dwordx4 a[232:235], v13, s[6:7] offset:2048
	global_load_dwordx4 a[236:239], v13, s[6:7] offset:3072
	v_add_u32_e32 v13, 0x1000, v13
	global_load_dwordx4 a[240:243], v13, s[6:7] offset:0
	global_load_dwordx4 a[244:247], v13, s[6:7] offset:1024
	global_load_dwordx4 a[248:251], v13, s[6:7] offset:2048
	global_load_dwordx4 a[252:255], v13, s[6:7] offset:3072
	s_mov_b32 m0, s28
	s_add_u32 s28, s28, 0x4000
	s_cmp_ge_u32 s28, s46
	s_cselect_b32 s28, s47, s28
	global_load_lds_dwordx4 v9, s[26:27]
	global_load_lds_dwordx4 v9, s[26:27] offset:1024
	s_add_u32 m0, m0, 0x800
	s_nop 0
	global_load_lds_dwordx4 v10, s[26:27]
	global_load_lds_dwordx4 v10, s[26:27] offset:1024
	s_add_u32 s26, s26, 0x800
	s_addc_u32 s27, s27, 0
	s_mov_b32 m0, s28
	s_add_u32 s28, s28, 0x4000
	s_cmp_ge_u32 s28, s46
	s_cselect_b32 s28, s47, s28
	global_load_lds_dwordx4 v9, s[26:27]
	global_load_lds_dwordx4 v9, s[26:27] offset:1024
	s_add_u32 m0, m0, 0x800
	s_nop 0
	global_load_lds_dwordx4 v10, s[26:27]
	global_load_lds_dwordx4 v10, s[26:27] offset:1024
	s_add_u32 s26, s26, 0x800
	s_addc_u32 s27, s27, 0
	s_waitcnt vmcnt(63)
	s_barrier
	v_add_u32_e32 v5, s29, v4
	v_xor_b32_e32 v6, 64, v5
	s_add_u32 s29, s29, 0x4000
	s_cmp_ge_u32 s29, 0x14000
	s_cselect_b32 s29, 0, s29
	ds_read_b128 v[128:131], v5 offset:0
	ds_read_b128 v[132:135], v6 offset:0
	ds_read_b128 v[136:139], v5 offset:2048
	ds_read_b128 v[140:143], v6 offset:2048
	ds_read_b128 v[144:147], v5 offset:4096
	ds_read_b128 v[148:151], v6 offset:4096
	ds_read_b128 v[152:155], v5 offset:6144
	ds_read_b128 v[156:159], v6 offset:6144
	ds_read_b128 v[160:163], v5 offset:8192
	ds_read_b128 v[164:167], v6 offset:8192
	ds_read_b128 v[168:171], v5 offset:10240
	ds_read_b128 v[172:175], v6 offset:10240
	ds_read_b128 v[176:179], v5 offset:12288
	ds_read_b128 v[180:183], v6 offset:12288
	ds_read_b128 v[184:187], v5 offset:14336
	ds_read_b128 v[188:191], v6 offset:14336
	s_waitcnt lgkmcnt(0)
	s_mov_b32 m0, s28
	s_add_u32 s28, s28, 0x4000
	s_cmp_ge_u32 s28, s46
	s_cselect_b32 s28, s47, s28
	global_load_lds_dwordx4 v9, s[26:27]
	global_load_lds_dwordx4 v9, s[26:27] offset:1024
	s_add_u32 m0, m0, 0x800
	s_nop 0
	global_load_lds_dwordx4 v10, s[26:27]
	global_load_lds_dwordx4 v10, s[26:27] offset:1024
	s_add_u32 s26, s26, 0x800
	s_addc_u32 s27, s27, 0
	v_add_u32_e32 v7, s29, v4
	v_xor_b32_e32 v8, 64, v7
	s_add_u32 s29, s29, 0x4000
	s_cmp_ge_u32 s29, 0x14000
	s_cselect_b32 s29, 0, s29
	s_waitcnt vmcnt(63)
	v_mfma_f32_16x16x32_f16 v[48:51], a[0:3], v[128:131], v[32:35]
	v_mfma_f32_16x16x32_f16 v[52:55], a[4:7], v[128:131], v[36:39]
	v_mfma_f32_16x16x32_f16 v[56:59], a[8:11], v[128:131], v[40:43]
	ds_read_b128 v[192:195], v7 offset:0
	v_mfma_f32_16x16x32_f16 v[60:63], a[12:15], v[128:131], v[44:47]
	ds_read_b128 v[196:199], v8 offset:0
	s_waitcnt vmcnt(63)
	v_mfma_f32_16x16x32_f16 v[48:51], a[16:19], v[132:135], v[48:51]
	ds_read_b128 v[200:203], v7 offset:2048
	v_mfma_f32_16x16x32_f16 v[52:55], a[20:23], v[132:135], v[52:55]
	ds_read_b128 v[204:207], v8 offset:2048
	v_mfma_f32_16x16x32_f16 v[56:59], a[24:27], v[132:135], v[56:59]
	ds_read_b128 v[208:211], v7 offset:4096
	v_mfma_f32_16x16x32_f16 v[60:63], a[28:31], v[132:135], v[60:63]
	ds_read_b128 v[212:215], v8 offset:4096
	s_waitcnt vmcnt(63)
	v_mfma_f32_16x16x32_f16 v[48:51], a[32:35], v[136:139], v[48:51]
	ds_read_b128 v[216:219], v7 offset:6144
	v_mfma_f32_16x16x32_f16 v[52:55], a[36:39], v[136:139], v[52:55]
	ds_read_b128 v[220:223], v8 offset:6144
	v_mfma_f32_16x16x32_f16 v[56:59], a[40:43], v[136:139], v[56:59]
	ds_read_b128 v[224:227], v7 offset:8192
	v_mfma_f32_16x16x32_f16 v[60:63], a[44:47], v[136:139], v[60:63]
	ds_read_b128 v[228:231], v8 offset:8192
	s_waitcnt vmcnt(60)
	v_mfma_f32_16x16x32_f16 v[48:51], a[48:51], v[140:143], v[48:51]
	ds_read_b128 v[232:235], v7 offset:10240
	v_mfma_f32_16x16x32_f16 v[52:55], a[52:55], v[140:143], v[52:55]
	ds_read_b128 v[236:239], v8 offset:10240
	v_mfma_f32_16x16x32_f16 v[56:59], a[56:59], v[140:143], v[56:59]
	ds_read_b128 v[240:243], v7 offset:12288
	v_mfma_f32_16x16x32_f16 v[60:63], a[60:63], v[140:143], v[60:63]
	ds_read_b128 v[244:247], v8 offset:12288
	s_waitcnt vmcnt(56)
	v_mfma_f32_16x16x32_f16 v[48:51], a[64:67], v[144:147], v[48:51]
	ds_read_b128 v[248:251], v7 offset:14336
	v_mfma_f32_16x16x32_f16 v[52:55], a[68:71], v[144:147], v[52:55]
	ds_read_b128 v[252:255], v8 offset:14336
	v_mfma_f32_16x16x32_f16 v[56:59], a[72:75], v[144:147], v[56:59]
	v_mfma_f32_16x16x32_f16 v[60:63], a[76:79], v[144:147], v[60:63]
	s_waitcnt vmcnt(52)
	v_mfma_f32_16x16x32_f16 v[48:51], a[80:83], v[148:151], v[48:51]
	v_mfma_f32_16x16x32_f16 v[52:55], a[84:87], v[148:151], v[52:55]
	v_mfma_f32_16x16x32_f16 v[56:59], a[88:91], v[148:151], v[56:59]
	v_mfma_f32_16x16x32_f16 v[60:63], a[92:95], v[148:151], v[60:63]
	s_waitcnt vmcnt(48)
	v_mfma_f32_16x16x32_f16 v[48:51], a[96:99], v[152:155], v[48:51]
	v_mfma_f32_16x16x32_f16 v[52:55], a[100:103], v[152:155], v[52:55]
	v_mfma_f32_16x16x32_f16 v[56:59], a[104:107], v[152:155], v[56:59]
	v_mfma_f32_16x16x32_f16 v[60:63], a[108:111], v[152:155], v[60:63]
	s_waitcnt vmcnt(44)
	v_mfma_f32_16x16x32_f16 v[48:51], a[112:115], v[156:159], v[48:51]
	v_mfma_f32_16x16x32_f16 v[52:55], a[116:119], v[156:159], v[52:55]
	v_mfma_f32_16x16x32_f16 v[56:59], a[120:123], v[156:159], v[56:59]
	v_mfma_f32_16x16x32_f16 v[60:63], a[124:127], v[156:159], v[60:63]
	s_waitcnt vmcnt(40)
	v_mfma_f32_16x16x32_f16 v[48:51], a[128:131], v[160:163], v[48:51]
	v_mfma_f32_16x16x32_f16 v[52:55], a[132:135], v[160:163], v[52:55]
	v_mfma_f32_16x16x32_f16 v[56:59], a[136:139], v[160:163], v[56:59]
	v_mfma_f32_16x16x32_f16 v[60:63], a[140:143], v[160:163], v[60:63]
	s_waitcnt vmcnt(36)
	v_mfma_f32_16x16x32_f16 v[48:51], a[144:147], v[164:167], v[48:51]
	v_mfma_f32_16x16x32_f16 v[52:55], a[148:151], v[164:167], v[52:55]
	v_mfma_f32_16x16x32_f16 v[56:59], a[152:155], v[164:167], v[56:59]
	v_mfma_f32_16x16x32_f16 v[60:63], a[156:159], v[164:167], v[60:63]
	s_waitcnt vmcnt(32)
	v_mfma_f32_16x16x32_f16 v[48:51], a[160:163], v[168:171], v[48:51]
	v_mfma_f32_16x16x32_f16 v[52:55], a[164:167], v[168:171], v[52:55]
	v_mfma_f32_16x16x32_f16 v[56:59], a[168:171], v[168:171], v[56:59]
	v_mfma_f32_16x16x32_f16 v[60:63], a[172:175], v[168:171], v[60:63]
	s_waitcnt vmcnt(28)
	v_mfma_f32_16x16x32_f16 v[48:51], a[176:179], v[172:175], v[48:51]
	v_mfma_f32_16x16x32_f16 v[52:55], a[180:183], v[172:175], v[52:55]
	v_mfma_f32_16x16x32_f16 v[56:59], a[184:187], v[172:175], v[56:59]
	v_mfma_f32_16x16x32_f16 v[60:63], a[188:191], v[172:175], v[60:63]
	s_waitcnt vmcnt(24)
	v_mfma_f32_16x16x32_f16 v[48:51], a[192:195], v[176:179], v[48:51]
	v_mfma_f32_16x16x32_f16 v[52:55], a[196:199], v[176:179], v[52:55]
	v_mfma_f32_16x16x32_f16 v[56:59], a[200:203], v[176:179], v[56:59]
	v_mfma_f32_16x16x32_f16 v[60:63], a[204:207], v[176:179], v[60:63]
	s_waitcnt vmcnt(20)
	v_mfma_f32_16x16x32_f16 v[48:51], a[208:211], v[180:183], v[48:51]
	v_mfma_f32_16x16x32_f16 v[52:55], a[212:215], v[180:183], v[52:55]
	v_mfma_f32_16x16x32_f16 v[56:59], a[216:219], v[180:183], v[56:59]
	v_mfma_f32_16x16x32_f16 v[60:63], a[220:223], v[180:183], v[60:63]
	s_waitcnt vmcnt(16)
	v_mfma_f32_16x16x32_f16 v[48:51], a[224:227], v[184:187], v[48:51]
	v_mfma_f32_16x16x32_f16 v[52:55], a[228:231], v[184:187], v[52:55]
	v_mfma_f32_16x16x32_f16 v[56:59], a[232:235], v[184:187], v[56:59]
	v_mfma_f32_16x16x32_f16 v[60:63], a[236:239], v[184:187], v[60:63]
	s_waitcnt vmcnt(12)
	v_mfma_f32_16x16x32_f16 v[48:51], a[240:243], v[188:191], v[48:51]
	v_mfma_f32_16x16x32_f16 v[52:55], a[244:247], v[188:191], v[52:55]
	v_mfma_f32_16x16x32_f16 v[56:59], a[248:251], v[188:191], v[56:59]
	v_mfma_f32_16x16x32_f16 v[60:63], a[252:255], v[188:191], v[60:63]
Lg1_loop:
	s_waitcnt vmcnt(8) lgkmcnt(0)
	s_barrier
	v_mfma_f32_16x16x32_f16 v[64:67], a[0:3], v[192:195], v[32:35]
	v_mfma_f32_16x16x32_f16 v[68:71], a[4:7], v[192:195], v[36:39]
	v_add_u32_e32 v5, s29, v4
	v_xor_b32_e32 v6, 64, v5
	s_add_u32 s29, s29, 0x4000
	s_cmp_ge_u32 s29, 0x14000
	s_cselect_b32 s29, 0, s29
	v_mfma_f32_16x16x32_f16 v[72:75], a[8:11], v[192:195], v[40:43]
	ds_read_b128 v[128:131], v5 offset:0
	v_mfma_f32_16x16x32_f16 v[76:79], a[12:15], v[192:195], v[44:47]
	ds_read_b128 v[132:135], v6 offset:0
	v_fma_f32 v16, |v48|, v113, s48
	v_fma_f32 v16, |v48|, v16, s49
	v_fma_f32 v16, |v48|, v16, s50
	v_fma_f32 v16, |v48|, v16, s51
	v_fma_f32 v16, |v48|, v16, s52
	v_mfma_f32_16x16x32_f16 v[64:67], a[16:19], v[196:199], v[64:67]
	ds_read_b128 v[136:139], v5 offset:2048
	v_fma_f32 v16, |v48|, v16, 1.0
	v_mul_f32_e32 v16, v16, v16
	v_mul_f32_e32 v16, v16, v16
	v_mul_f32_e32 v16, v16, v16
	v_mfma_f32_16x16x32_f16 v[68:71], a[20:23], v[196:199], v[68:71]
	ds_read_b128 v[140:143], v6 offset:2048
	v_mul_f32_e32 v16, v16, v16
	v_rcp_f32_e32 v16, v16
	v_max_f32_e32 v17, 0, v48
	v_mul_f32_e64 v18, |v48|, v16
	v_mfma_f32_16x16x32_f16 v[72:75], a[24:27], v[196:199], v[72:75]
	ds_read_b128 v[144:147], v5 offset:4096
	v_fmamk_f32 v96, v18, 0xbf000000, v17
	v_fma_f32 v19, |v49|, v113, s48
	v_fma_f32 v19, |v49|, v19, s49
	v_fma_f32 v19, |v49|, v19, s50
	v_mfma_f32_16x16x32_f16 v[76:79], a[28:31], v[196:199], v[76:79]
	ds_read_b128 v[148:151], v6 offset:4096
	v_fma_f32 v19, |v49|, v19, s51
	v_fma_f32 v19, |v49|, v19, s52
	v_fma_f32 v19, |v49|, v19, 1.0
	v_mul_f32_e32 v19, v19, v19
	v_mfma_f32_16x16x32_f16 v[64:67], a[32:35], v[200:203], v[64:67]
	ds_read_b128 v[152:155], v5 offset:6144
	v_mul_f32_e32 v19, v19, v19
	v_mul_f32_e32 v19, v19, v19
	v_mul_f32_e32 v19, v19, v19
	v_rcp_f32_e32 v19, v19
	v_max_f32_e32 v20, 0, v49
	v_mfma_f32_16x16x32_f16 v[68:71], a[36:39], v[200:203], v[68:71]
	ds_read_b128 v[156:159], v6 offset:6144
	v_mul_f32_e64 v21, |v49|, v19
	v_fmamk_f32 v97, v21, 0xbf000000, v20
	v_fma_f32 v22, |v50|, v113, s48
	v_fma_f32 v22, |v50|, v22, s49
	v_mfma_f32_16x16x32_f16 v[72:75], a[40:43], v[200:203], v[72:75]
	ds_read_b128 v[160:163], v5 offset:8192
	v_fma_f32 v22, |v50|, v22, s50
	v_fma_f32 v22, |v50|, v22, s51
	v_fma_f32 v22, |v50|, v22, s52
	v_fma_f32 v22, |v50|, v22, 1.0
	v_mfma_f32_16x16x32_f16 v[76:79], a[44:47], v[200:203], v[76:79]
	ds_read_b128 v[164:167], v6 offset:8192
	v_mul_f32_e32 v22, v22, v22
	v_mul_f32_e32 v22, v22, v22
	v_mul_f32_e32 v22, v22, v22
	v_mul_f32_e32 v22, v22, v22
	v_mfma_f32_16x16x32_f16 v[64:67], a[48:51], v[204:207], v[64:67]
	ds_read_b128 v[168:171], v5 offset:10240
	v_rcp_f32_e32 v22, v22
	v_max_f32_e32 v23, 0, v50
	v_mul_f32_e64 v24, |v50|, v22
	v_fmamk_f32 v98, v24, 0xbf000000, v23
	v_mfma_f32_16x16x32_f16 v[68:71], a[52:55], v[204:207], v[68:71]
	ds_read_b128 v[172:175], v6 offset:10240
	v_fma_f32 v25, |v51|, v113, s48
	v_fma_f32 v25, |v51|, v25, s49
	v_fma_f32 v25, |v51|, v25, s50
	v_fma_f32 v25, |v51|, v25, s51
	v_mfma_f32_16x16x32_f16 v[72:75], a[56:59], v[204:207], v[72:75]
	ds_read_b128 v[176:179], v5 offset:12288
	v_fma_f32 v25, |v51|, v25, s52
	v_fma_f32 v25, |v51|, v25, 1.0
	v_mul_f32_e32 v25, v25, v25
	v_mul_f32_e32 v25, v25, v25
	v_mul_f32_e32 v25, v25, v25
	v_mfma_f32_16x16x32_f16 v[76:79], a[60:63], v[204:207], v[76:79]
	ds_read_b128 v[180:183], v6 offset:12288
	v_mul_f32_e32 v25, v25, v25
	v_rcp_f32_e32 v25, v25
	v_max_f32_e32 v26, 0, v51
	v_mul_f32_e64 v27, |v51|, v25
	v_mfma_f32_16x16x32_f16 v[64:67], a[64:67], v[208:211], v[64:67]
	ds_read_b128 v[184:187], v5 offset:14336
	v_fmamk_f32 v99, v27, 0xbf000000, v26
	v_fma_f32 v16, |v52|, v113, s48
	v_fma_f32 v16, |v52|, v16, s49
	v_fma_f32 v16, |v52|, v16, s50
	v_mfma_f32_16x16x32_f16 v[68:71], a[68:71], v[208:211], v[68:71]
	ds_read_b128 v[188:191], v6 offset:14336
	v_fma_f32 v16, |v52|, v16, s51
	v_fma_f32 v16, |v52|, v16, s52
	v_fma_f32 v16, |v52|, v16, 1.0
	v_mul_f32_e32 v16, v16, v16
	v_mfma_f32_16x16x32_f16 v[72:75], a[72:75], v[208:211], v[72:75]
	v_mul_f32_e32 v16, v16, v16
	v_mul_f32_e32 v16, v16, v16
	v_mul_f32_e32 v16, v16, v16
	v_rcp_f32_e32 v16, v16
	v_mfma_f32_16x16x32_f16 v[76:79], a[76:79], v[208:211], v[76:79]
	v_max_f32_e32 v17, 0, v52
	v_mul_f32_e64 v18, |v52|, v16
	v_fmamk_f32 v100, v18, 0xbf000000, v17
	v_fma_f32 v19, |v53|, v113, s48
	v_fma_f32 v19, |v53|, v19, s49
	v_mfma_f32_16x16x32_f16 v[64:67], a[80:83], v[212:215], v[64:67]
	v_fma_f32 v19, |v53|, v19, s50
	v_fma_f32 v19, |v53|, v19, s51
	v_fma_f32 v19, |v53|, v19, s52
	v_fma_f32 v19, |v53|, v19, 1.0
	v_mfma_f32_16x16x32_f16 v[68:71], a[84:87], v[212:215], v[68:71]
	v_mul_f32_e32 v19, v19, v19
	v_mul_f32_e32 v19, v19, v19
	v_mul_f32_e32 v19, v19, v19
	v_mul_f32_e32 v19, v19, v19
	v_mfma_f32_16x16x32_f16 v[72:75], a[88:91], v[212:215], v[72:75]
	s_mov_b32 m0, s28
	s_add_u32 s28, s28, 0x4000
	s_cmp_ge_u32 s28, s46
	s_cselect_b32 s28, s47, s28
	global_load_lds_dwordx4 v9, s[26:27]
	v_rcp_f32_e32 v19, v19
	v_max_f32_e32 v20, 0, v53
	v_mul_f32_e64 v21, |v53|, v19
	v_fmamk_f32 v101, v21, 0xbf000000, v20
	v_mfma_f32_16x16x32_f16 v[76:79], a[92:95], v[212:215], v[76:79]
	v_fma_f32 v22, |v54|, v113, s48
	v_fma_f32 v22, |v54|, v22, s49
	v_fma_f32 v22, |v54|, v22, s50
	v_fma_f32 v22, |v54|, v22, s51
	v_mfma_f32_16x16x32_f16 v[64:67], a[96:99], v[216:219], v[64:67]
	v_fma_f32 v22, |v54|, v22, s52
	v_fma_f32 v22, |v54|, v22, 1.0
	v_mul_f32_e32 v22, v22, v22
	v_mul_f32_e32 v22, v22, v22
	v_mfma_f32_16x16x32_f16 v[68:71], a[100:103], v[216:219], v[68:71]
	v_mul_f32_e32 v22, v22, v22
	v_mul_f32_e32 v22, v22, v22
	v_rcp_f32_e32 v22, v22
	v_max_f32_e32 v23, 0, v54
	v_mul_f32_e64 v24, |v54|, v22
	v_mfma_f32_16x16x32_f16 v[72:75], a[104:107], v[216:219], v[72:75]
	v_fmamk_f32 v102, v24, 0xbf000000, v23
	v_fma_f32 v25, |v55|, v113, s48
	v_fma_f32 v25, |v55|, v25, s49
	v_fma_f32 v25, |v55|, v25, s50
	v_mfma_f32_16x16x32_f16 v[76:79], a[108:111], v[216:219], v[76:79]
	v_fma_f32 v25, |v55|, v25, s51
	v_fma_f32 v25, |v55|, v25, s52
	v_fma_f32 v25, |v55|, v25, 1.0
	v_mul_f32_e32 v25, v25, v25
	v_mfma_f32_16x16x32_f16 v[64:67], a[112:115], v[220:223], v[64:67]
	v_mul_f32_e32 v25, v25, v25
	v_mul_f32_e32 v25, v25, v25
	v_mul_f32_e32 v25, v25, v25
	v_rcp_f32_e32 v25, v25
	v_mfma_f32_16x16x32_f16 v[68:71], a[116:119], v[220:223], v[68:71]
	v_max_f32_e32 v26, 0, v55
	v_mul_f32_e64 v27, |v55|, v25
	v_fmamk_f32 v103, v27, 0xbf000000, v26
	v_fma_f32 v16, |v56|, v113, s48
	v_mfma_f32_16x16x32_f16 v[72:75], a[120:123], v[220:223], v[72:75]
	v_fma_f32 v16, |v56|, v16, s49
	v_fma_f32 v16, |v56|, v16, s50
	v_fma_f32 v16, |v56|, v16, s51
	v_fma_f32 v16, |v56|, v16, s52
	v_mfma_f32_16x16x32_f16 v[76:79], a[124:127], v[220:223], v[76:79]
	v_fma_f32 v16, |v56|, v16, 1.0
	v_mul_f32_e32 v16, v16, v16
	v_mul_f32_e32 v16, v16, v16
	v_mul_f32_e32 v16, v16, v16
	v_mul_f32_e32 v16, v16, v16
	v_mfma_f32_16x16x32_f16 v[64:67], a[128:131], v[224:227], v[64:67]
	v_rcp_f32_e32 v16, v16
	v_max_f32_e32 v17, 0, v56
	v_mul_f32_e64 v18, |v56|, v16
	v_fmamk_f32 v104, v18, 0xbf000000, v17
	v_mfma_f32_16x16x32_f16 v[68:71], a[132:135], v[224:227], v[68:71]
	global_load_lds_dwordx4 v9, s[26:27] offset:1024
	v_fma_f32 v19, |v57|, v113, s48
	v_fma_f32 v19, |v57|, v19, s49
	v_fma_f32 v19, |v57|, v19, s50
	v_fma_f32 v19, |v57|, v19, s51
	v_mfma_f32_16x16x32_f16 v[72:75], a[136:139], v[224:227], v[72:75]
	v_fma_f32 v19, |v57|, v19, s52
	v_fma_f32 v19, |v57|, v19, 1.0
	v_mul_f32_e32 v19, v19, v19
	v_mul_f32_e32 v19, v19, v19
	v_mfma_f32_16x16x32_f16 v[76:79], a[140:143], v[224:227], v[76:79]
	v_mul_f32_e32 v19, v19, v19
	v_mul_f32_e32 v19, v19, v19
	v_rcp_f32_e32 v19, v19
	v_max_f32_e32 v20, 0, v57
	v_mfma_f32_16x16x32_f16 v[64:67], a[144:147], v[228:231], v[64:67]
	v_mul_f32_e64 v21, |v57|, v19
	v_fmamk_f32 v105, v21, 0xbf000000, v20
	v_fma_f32 v22, |v58|, v113, s48
	v_fma_f32 v22, |v58|, v22, s49
	v_fma_f32 v22, |v58|, v22, s50
	v_mfma_f32_16x16x32_f16 v[68:71], a[148:151], v[228:231], v[68:71]
	v_fma_f32 v22, |v58|, v22, s51
	v_fma_f32 v22, |v58|, v22, s52
	v_fma_f32 v22, |v58|, v22, 1.0
	v_mul_f32_e32 v22, v22, v22
	v_mfma_f32_16x16x32_f16 v[72:75], a[152:155], v[228:231], v[72:75]
	v_mul_f32_e32 v22, v22, v22
	v_mul_f32_e32 v22, v22, v22
	v_mul_f32_e32 v22, v22, v22
	v_rcp_f32_e32 v22, v22
	v_mfma_f32_16x16x32_f16 v[76:79], a[156:159], v[228:231], v[76:79]
	v_max_f32_e32 v23, 0, v58
	v_mul_f32_e64 v24, |v58|, v22
	v_fmamk_f32 v106, v24, 0xbf000000, v23
	v_fma_f32 v25, |v59|, v113, s48
	v_mfma_f32_16x16x32_f16 v[64:67], a[160:163], v[232:235], v[64:67]
	v_fma_f32 v25, |v59|, v25, s49
	v_fma_f32 v25, |v59|, v25, s50
	v_fma_f32 v25, |v59|, v25, s51
	v_fma_f32 v25, |v59|, v25, s52
	v_mfma_f32_16x16x32_f16 v[68:71], a[164:167], v[232:235], v[68:71]
	v_fma_f32 v25, |v59|, v25, 1.0
	v_mul_f32_e32 v25, v25, v25
	v_mul_f32_e32 v25, v25, v25
	v_mul_f32_e32 v25, v25, v25
	v_mfma_f32_16x16x32_f16 v[72:75], a[168:171], v[232:235], v[72:75]
	v_mul_f32_e32 v25, v25, v25
	v_rcp_f32_e32 v25, v25
	v_max_f32_e32 v26, 0, v59
	v_mul_f32_e64 v27, |v59|, v25
	v_fmamk_f32 v107, v27, 0xbf000000, v26
	v_mfma_f32_16x16x32_f16 v[76:79], a[172:175], v[232:235], v[76:79]
	v_fma_f32 v16, |v60|, v113, s48
	v_fma_f32 v16, |v60|, v16, s49
	v_fma_f32 v16, |v60|, v16, s50
	v_fma_f32 v16, |v60|, v16, s51
	v_mfma_f32_16x16x32_f16 v[64:67], a[176:179], v[236:239], v[64:67]
	s_add_u32 m0, m0, 0x800
	s_nop 0
	global_load_lds_dwordx4 v10, s[26:27]
	v_fma_f32 v16, |v60|, v16, s52
	v_fma_f32 v16, |v60|, v16, 1.0
	v_mul_f32_e32 v16, v16, v16
	v_mul_f32_e32 v16, v16, v16
	v_mfma_f32_16x16x32_f16 v[68:71], a[180:183], v[236:239], v[68:71]
	v_mul_f32_e32 v16, v16, v16
	v_mul_f32_e32 v16, v16, v16
	v_rcp_f32_e32 v16, v16
	v_max_f32_e32 v17, 0, v60
	v_mfma_f32_16x16x32_f16 v[72:75], a[184:187], v[236:239], v[72:75]
	v_mul_f32_e64 v18, |v60|, v16
	v_fmamk_f32 v108, v18, 0xbf000000, v17
	v_fma_f32 v19, |v61|, v113, s48
	v_fma_f32 v19, |v61|, v19, s49
	v_mfma_f32_16x16x32_f16 v[76:79], a[188:191], v[236:239], v[76:79]
	v_fma_f32 v19, |v61|, v19, s50
	v_fma_f32 v19, |v61|, v19, s51
	v_fma_f32 v19, |v61|, v19, s52
	v_fma_f32 v19, |v61|, v19, 1.0
	v_mul_f32_e32 v19, v19, v19
	v_mfma_f32_16x16x32_f16 v[64:67], a[192:195], v[240:243], v[64:67]
	v_mul_f32_e32 v19, v19, v19
	v_mul_f32_e32 v19, v19, v19
	v_mul_f32_e32 v19, v19, v19
	v_rcp_f32_e32 v19, v19
	v_mfma_f32_16x16x32_f16 v[68:71], a[196:199], v[240:243], v[68:71]
	v_max_f32_e32 v20, 0, v61
	v_mul_f32_e64 v21, |v61|, v19
	v_fmamk_f32 v109, v21, 0xbf000000, v20
	v_fma_f32 v22, |v62|, v113, s48
	v_mfma_f32_16x16x32_f16 v[72:75], a[200:203], v[240:243], v[72:75]
	v_fma_f32 v22, |v62|, v22, s49
	v_fma_f32 v22, |v62|, v22, s50
	v_fma_f32 v22, |v62|, v22, s51
	v_fma_f32 v22, |v62|, v22, s52
	v_mfma_f32_16x16x32_f16 v[76:79], a[204:207], v[240:243], v[76:79]
	v_fma_f32 v22, |v62|, v22, 1.0
	v_mul_f32_e32 v22, v22, v22
	v_mul_f32_e32 v22, v22, v22
	v_mul_f32_e32 v22, v22, v22
	v_mfma_f32_16x16x32_f16 v[64:67], a[208:211], v[244:247], v[64:67]
	v_mul_f32_e32 v22, v22, v22
	v_rcp_f32_e32 v22, v22
	v_max_f32_e32 v23, 0, v62
	v_mul_f32_e64 v24, |v62|, v22
	v_mfma_f32_16x16x32_f16 v[68:71], a[212:215], v[244:247], v[68:71]
	v_fmamk_f32 v110, v24, 0xbf000000, v23
	v_fma_f32 v25, |v63|, v113, s48
	v_fma_f32 v25, |v63|, v25, s49
	v_fma_f32 v25, |v63|, v25, s50
	v_fma_f32 v25, |v63|, v25, s51
	v_mfma_f32_16x16x32_f16 v[72:75], a[216:219], v[244:247], v[72:75]
	v_fma_f32 v25, |v63|, v25, s52
	v_fma_f32 v25, |v63|, v25, 1.0
	v_mul_f32_e32 v25, v25, v25
	v_mul_f32_e32 v25, v25, v25
	v_mfma_f32_16x16x32_f16 v[76:79], a[220:223], v[244:247], v[76:79]
	v_mul_f32_e32 v25, v25, v25
	v_mul_f32_e32 v25, v25, v25
	v_rcp_f32_e32 v25, v25
	v_max_f32_e32 v26, 0, v63
	v_mfma_f32_16x16x32_f16 v[64:67], a[224:227], v[248:251], v[64:67]
	global_load_lds_dwordx4 v10, s[26:27] offset:1024
	v_mul_f32_e64 v27, |v63|, v25
	v_fmamk_f32 v111, v27, 0xbf000000, v26
	v_cvt_pk_f16_f32 v96, v96, v97
	v_cvt_pk_f16_f32 v97, v98, v99
	v_mfma_f32_16x16x32_f16 v[68:71], a[228:231], v[248:251], v[68:71]
	s_add_u32 s26, s26, 0x800
	s_addc_u32 s27, s27, 0
	v_cvt_pk_f16_f32 v98, v100, v101
	v_cvt_pk_f16_f32 v99, v102, v103
	v_cvt_pk_f16_f32 v100, v104, v105
	v_cvt_pk_f16_f32 v101, v106, v107
	v_mfma_f32_16x16x32_f16 v[72:75], a[232:235], v[248:251], v[72:75]
	v_cvt_pk_f16_f32 v102, v108, v109
	v_cvt_pk_f16_f32 v103, v110, v111
	global_store_dwordx4 v14, v[96:99], s[30:31]
	global_store_dwordx4 v14, v[100:103], s[30:31] offset:16
	v_mfma_f32_16x16x32_f16 v[76:79], a[236:239], v[248:251], v[76:79]
	s_add_u32 s30, s30, 0x800
	s_addc_u32 s31, s31, 0
	v_mfma_f32_16x16x32_f16 v[64:67], a[240:243], v[252:255], v[64:67]
	v_mfma_f32_16x16x32_f16 v[68:71], a[244:247], v[252:255], v[68:71]
	v_mfma_f32_16x16x32_f16 v[72:75], a[248:251], v[252:255], v[72:75]
	v_mfma_f32_16x16x32_f16 v[76:79], a[252:255], v[252:255], v[76:79]
	s_sub_u32 s24, s24, 1
	s_cmp_le_u32 s24, 1
	s_cbranch_scc1 Lg1_exitA
	s_waitcnt vmcnt(8) lgkmcnt(0)
	s_barrier
	v_mfma_f32_16x16x32_f16 v[48:51], a[0:3], v[128:131], v[32:35]
	v_mfma_f32_16x16x32_f16 v[52:55], a[4:7], v[128:131], v[36:39]
	v_add_u32_e32 v7, s29, v4
	v_xor_b32_e32 v8, 64, v7
	s_add_u32 s29, s29, 0x4000
	s_cmp_ge_u32 s29, 0x14000
	s_cselect_b32 s29, 0, s29
	v_mfma_f32_16x16x32_f16 v[56:59], a[8:11], v[128:131], v[40:43]
	ds_read_b128 v[192:195], v7 offset:0
	v_mfma_f32_16x16x32_f16 v[60:63], a[12:15], v[128:131], v[44:47]
	ds_read_b128 v[196:199], v8 offset:0
	v_fma_f32 v16, |v64|, v113, s48
	v_fma_f32 v16, |v64|, v16, s49
	v_fma_f32 v16, |v64|, v16, s50
	v_fma_f32 v16, |v64|, v16, s51
	v_fma_f32 v16, |v64|, v16, s52
	v_mfma_f32_16x16x32_f16 v[48:51], a[16:19], v[132:135], v[48:51]
	ds_read_b128 v[200:203], v7 offset:2048
	v_fma_f32 v16, |v64|, v16, 1.0
	v_mul_f32_e32 v16, v16, v16
	v_mul_f32_e32 v16, v16, v16
	v_mul_f32_e32 v16, v16, v16
	v_mfma_f32_16x16x32_f16 v[52:55], a[20:23], v[132:135], v[52:55]
	ds_read_b128 v[204:207], v8 offset:2048
	v_mul_f32_e32 v16, v16, v16
	v_rcp_f32_e32 v16, v16
	v_max_f32_e32 v17, 0, v64
	v_mul_f32_e64 v18, |v64|, v16
	v_mfma_f32_16x16x32_f16 v[56:59], a[24:27], v[132:135], v[56:59]
	ds_read_b128 v[208:211], v7 offset:4096
	v_fmamk_f32 v96, v18, 0xbf000000, v17
	v_fma_f32 v19, |v65|, v113, s48
	v_fma_f32 v19, |v65|, v19, s49
	v_fma_f32 v19, |v65|, v19, s50
	v_mfma_f32_16x16x32_f16 v[60:63], a[28:31], v[132:135], v[60:63]
	ds_read_b128 v[212:215], v8 offset:4096
	v_fma_f32 v19, |v65|, v19, s51
	v_fma_f32 v19, |v65|, v19, s52
	v_fma_f32 v19, |v65|, v19, 1.0
	v_mul_f32_e32 v19, v19, v19
	v_mfma_f32_16x16x32_f16 v[48:51], a[32:35], v[136:139], v[48:51]
	ds_read_b128 v[216:219], v7 offset:6144
	v_mul_f32_e32 v19, v19, v19
	v_mul_f32_e32 v19, v19, v19
	v_mul_f32_e32 v19, v19, v19
	v_rcp_f32_e32 v19, v19
	v_max_f32_e32 v20, 0, v65
	v_mfma_f32_16x16x32_f16 v[52:55], a[36:39], v[136:139], v[52:55]
	ds_read_b128 v[220:223], v8 offset:6144
	v_mul_f32_e64 v21, |v65|, v19
	v_fmamk_f32 v97, v21, 0xbf000000, v20
	v_fma_f32 v22, |v66|, v113, s48
	v_fma_f32 v22, |v66|, v22, s49
	v_mfma_f32_16x16x32_f16 v[56:59], a[40:43], v[136:139], v[56:59]
	ds_read_b128 v[224:227], v7 offset:8192
	v_fma_f32 v22, |v66|, v22, s50
	v_fma_f32 v22, |v66|, v22, s51
	v_fma_f32 v22, |v66|, v22, s52
	v_fma_f32 v22, |v66|, v22, 1.0
	v_mfma_f32_16x16x32_f16 v[60:63], a[44:47], v[136:139], v[60:63]
	ds_read_b128 v[228:231], v8 offset:8192
	v_mul_f32_e32 v22, v22, v22
	v_mul_f32_e32 v22, v22, v22
	v_mul_f32_e32 v22, v22, v22
	v_mul_f32_e32 v22, v22, v22
	v_mfma_f32_16x16x32_f16 v[48:51], a[48:51], v[140:143], v[48:51]
	ds_read_b128 v[232:235], v7 offset:10240
	v_rcp_f32_e32 v22, v22
	v_max_f32_e32 v23, 0, v66
	v_mul_f32_e64 v24, |v66|, v22
	v_fmamk_f32 v98, v24, 0xbf000000, v23
	v_mfma_f32_16x16x32_f16 v[52:55], a[52:55], v[140:143], v[52:55]
	ds_read_b128 v[236:239], v8 offset:10240
	v_fma_f32 v25, |v67|, v113, s48
	v_fma_f32 v25, |v67|, v25, s49
	v_fma_f32 v25, |v67|, v25, s50
	v_fma_f32 v25, |v67|, v25, s51
	v_mfma_f32_16x16x32_f16 v[56:59], a[56:59], v[140:143], v[56:59]
	ds_read_b128 v[240:243], v7 offset:12288
	v_fma_f32 v25, |v67|, v25, s52
	v_fma_f32 v25, |v67|, v25, 1.0
	v_mul_f32_e32 v25, v25, v25
	v_mul_f32_e32 v25, v25, v25
	v_mul_f32_e32 v25, v25, v25
	v_mfma_f32_16x16x32_f16 v[60:63], a[60:63], v[140:143], v[60:63]
	ds_read_b128 v[244:247], v8 offset:12288
	v_mul_f32_e32 v25, v25, v25
	v_rcp_f32_e32 v25, v25
	v_max_f32_e32 v26, 0, v67
	v_mul_f32_e64 v27, |v67|, v25
	v_mfma_f32_16x16x32_f16 v[48:51], a[64:67], v[144:147], v[48:51]
	ds_read_b128 v[248:251], v7 offset:14336
	v_fmamk_f32 v99, v27, 0xbf000000, v26
	v_fma_f32 v16, |v68|, v113, s48
	v_fma_f32 v16, |v68|, v16, s49
	v_fma_f32 v16, |v68|, v16, s50
	v_mfma_f32_16x16x32_f16 v[52:55], a[68:71], v[144:147], v[52:55]
	ds_read_b128 v[252:255], v8 offset:14336
	v_fma_f32 v16, |v68|, v16, s51
	v_fma_f32 v16, |v68|, v16, s52
	v_fma_f32 v16, |v68|, v16, 1.0
	v_mul_f32_e32 v16, v16, v16
	v_mfma_f32_16x16x32_f16 v[56:59], a[72:75], v[144:147], v[56:59]
	v_mul_f32_e32 v16, v16, v16
	v_mul_f32_e32 v16, v16, v16
	v_mul_f32_e32 v16, v16, v16
	v_rcp_f32_e32 v16, v16
	v_mfma_f32_16x16x32_f16 v[60:63], a[76:79], v[144:147], v[60:63]
	v_max_f32_e32 v17, 0, v68
	v_mul_f32_e64 v18, |v68|, v16
	v_fmamk_f32 v100, v18, 0xbf000000, v17
	v_fma_f32 v19, |v69|, v113, s48
	v_fma_f32 v19, |v69|, v19, s49
	v_mfma_f32_16x16x32_f16 v[48:51], a[80:83], v[148:151], v[48:51]
	v_fma_f32 v19, |v69|, v19, s50
	v_fma_f32 v19, |v69|, v19, s51
	v_fma_f32 v19, |v69|, v19, s52
	v_fma_f32 v19, |v69|, v19, 1.0
	v_mfma_f32_16x16x32_f16 v[52:55], a[84:87], v[148:151], v[52:55]
	v_mul_f32_e32 v19, v19, v19
	v_mul_f32_e32 v19, v19, v19
	v_mul_f32_e32 v19, v19, v19
	v_mul_f32_e32 v19, v19, v19
	v_mfma_f32_16x16x32_f16 v[56:59], a[88:91], v[148:151], v[56:59]
	s_mov_b32 m0, s28
	s_add_u32 s28, s28, 0x4000
	s_cmp_ge_u32 s28, s46
	s_cselect_b32 s28, s47, s28
	global_load_lds_dwordx4 v9, s[26:27]
	v_rcp_f32_e32 v19, v19
	v_max_f32_e32 v20, 0, v69
	v_mul_f32_e64 v21, |v69|, v19
	v_fmamk_f32 v101, v21, 0xbf000000, v20
	v_mfma_f32_16x16x32_f16 v[60:63], a[92:95], v[148:151], v[60:63]
	v_fma_f32 v22, |v70|, v113, s48
	v_fma_f32 v22, |v70|, v22, s49
	v_fma_f32 v22, |v70|, v22, s50
	v_fma_f32 v22, |v70|, v22, s51
	v_mfma_f32_16x16x32_f16 v[48:51], a[96:99], v[152:155], v[48:51]
	v_fma_f32 v22, |v70|, v22, s52
	v_fma_f32 v22, |v70|, v22, 1.0
	v_mul_f32_e32 v22, v22, v22
	v_mul_f32_e32 v22, v22, v22
	v_mfma_f32_16x16x32_f16 v[52:55], a[100:103], v[152:155], v[52:55]
	v_mul_f32_e32 v22, v22, v22
	v_mul_f32_e32 v22, v22, v22
	v_rcp_f32_e32 v22, v22
	v_max_f32_e32 v23, 0, v70
	v_mul_f32_e64 v24, |v70|, v22
	v_mfma_f32_16x16x32_f16 v[56:59], a[104:107], v[152:155], v[56:59]
	v_fmamk_f32 v102, v24, 0xbf000000, v23
	v_fma_f32 v25, |v71|, v113, s48
	v_fma_f32 v25, |v71|, v25, s49
	v_fma_f32 v25, |v71|, v25, s50
	v_mfma_f32_16x16x32_f16 v[60:63], a[108:111], v[152:155], v[60:63]
	v_fma_f32 v25, |v71|, v25, s51
	v_fma_f32 v25, |v71|, v25, s52
	v_fma_f32 v25, |v71|, v25, 1.0
	v_mul_f32_e32 v25, v25, v25
	v_mfma_f32_16x16x32_f16 v[48:51], a[112:115], v[156:159], v[48:51]
	v_mul_f32_e32 v25, v25, v25
	v_mul_f32_e32 v25, v25, v25
	v_mul_f32_e32 v25, v25, v25
	v_rcp_f32_e32 v25, v25
	v_mfma_f32_16x16x32_f16 v[52:55], a[116:119], v[156:159], v[52:55]
	v_max_f32_e32 v26, 0, v71
	v_mul_f32_e64 v27, |v71|, v25
	v_fmamk_f32 v103, v27, 0xbf000000, v26
	v_fma_f32 v16, |v72|, v113, s48
	v_mfma_f32_16x16x32_f16 v[56:59], a[120:123], v[156:159], v[56:59]
	v_fma_f32 v16, |v72|, v16, s49
	v_fma_f32 v16, |v72|, v16, s50
	v_fma_f32 v16, |v72|, v16, s51
	v_fma_f32 v16, |v72|, v16, s52
	v_mfma_f32_16x16x32_f16 v[60:63], a[124:127], v[156:159], v[60:63]
	v_fma_f32 v16, |v72|, v16, 1.0
	v_mul_f32_e32 v16, v16, v16
	v_mul_f32_e32 v16, v16, v16
	v_mul_f32_e32 v16, v16, v16
	v_mul_f32_e32 v16, v16, v16
	v_mfma_f32_16x16x32_f16 v[48:51], a[128:131], v[160:163], v[48:51]
	v_rcp_f32_e32 v16, v16
	v_max_f32_e32 v17, 0, v72
	v_mul_f32_e64 v18, |v72|, v16
	v_fmamk_f32 v104, v18, 0xbf000000, v17
	v_mfma_f32_16x16x32_f16 v[52:55], a[132:135], v[160:163], v[52:55]
	global_load_lds_dwordx4 v9, s[26:27] offset:1024
	v_fma_f32 v19, |v73|, v113, s48
	v_fma_f32 v19, |v73|, v19, s49
	v_fma_f32 v19, |v73|, v19, s50
	v_fma_f32 v19, |v73|, v19, s51
	v_mfma_f32_16x16x32_f16 v[56:59], a[136:139], v[160:163], v[56:59]
	v_fma_f32 v19, |v73|, v19, s52
	v_fma_f32 v19, |v73|, v19, 1.0
	v_mul_f32_e32 v19, v19, v19
	v_mul_f32_e32 v19, v19, v19
	v_mfma_f32_16x16x32_f16 v[60:63], a[140:143], v[160:163], v[60:63]
	v_mul_f32_e32 v19, v19, v19
	v_mul_f32_e32 v19, v19, v19
	v_rcp_f32_e32 v19, v19
	v_max_f32_e32 v20, 0, v73
	v_mfma_f32_16x16x32_f16 v[48:51], a[144:147], v[164:167], v[48:51]
	v_mul_f32_e64 v21, |v73|, v19
	v_fmamk_f32 v105, v21, 0xbf000000, v20
	v_fma_f32 v22, |v74|, v113, s48
	v_fma_f32 v22, |v74|, v22, s49
	v_fma_f32 v22, |v74|, v22, s50
	v_mfma_f32_16x16x32_f16 v[52:55], a[148:151], v[164:167], v[52:55]
	v_fma_f32 v22, |v74|, v22, s51
	v_fma_f32 v22, |v74|, v22, s52
	v_fma_f32 v22, |v74|, v22, 1.0
	v_mul_f32_e32 v22, v22, v22
	v_mfma_f32_16x16x32_f16 v[56:59], a[152:155], v[164:167], v[56:59]
	v_mul_f32_e32 v22, v22, v22
	v_mul_f32_e32 v22, v22, v22
	v_mul_f32_e32 v22, v22, v22
	v_rcp_f32_e32 v22, v22
	v_mfma_f32_16x16x32_f16 v[60:63], a[156:159], v[164:167], v[60:63]
	v_max_f32_e32 v23, 0, v74
	v_mul_f32_e64 v24, |v74|, v22
	v_fmamk_f32 v106, v24, 0xbf000000, v23
	v_fma_f32 v25, |v75|, v113, s48
	v_mfma_f32_16x16x32_f16 v[48:51], a[160:163], v[168:171], v[48:51]
	v_fma_f32 v25, |v75|, v25, s49
	v_fma_f32 v25, |v75|, v25, s50
	v_fma_f32 v25, |v75|, v25, s51
	v_fma_f32 v25, |v75|, v25, s52
	v_mfma_f32_16x16x32_f16 v[52:55], a[164:167], v[168:171], v[52:55]
	v_fma_f32 v25, |v75|, v25, 1.0
	v_mul_f32_e32 v25, v25, v25
	v_mul_f32_e32 v25, v25, v25
	v_mul_f32_e32 v25, v25, v25
	v_mfma_f32_16x16x32_f16 v[56:59], a[168:171], v[168:171], v[56:59]
	v_mul_f32_e32 v25, v25, v25
	v_rcp_f32_e32 v25, v25
	v_max_f32_e32 v26, 0, v75
	v_mul_f32_e64 v27, |v75|, v25
	v_fmamk_f32 v107, v27, 0xbf000000, v26
	v_mfma_f32_16x16x32_f16 v[60:63], a[172:175], v[168:171], v[60:63]
	v_fma_f32 v16, |v76|, v113, s48
	v_fma_f32 v16, |v76|, v16, s49
	v_fma_f32 v16, |v76|, v16, s50
	v_fma_f32 v16, |v76|, v16, s51
	v_mfma_f32_16x16x32_f16 v[48:51], a[176:179], v[172:175], v[48:51]
	s_add_u32 m0, m0, 0x800
	s_nop 0
	global_load_lds_dwordx4 v10, s[26:27]
	v_fma_f32 v16, |v76|, v16, s52
	v_fma_f32 v16, |v76|, v16, 1.0
	v_mul_f32_e32 v16, v16, v16
	v_mul_f32_e32 v16, v16, v16
	v_mfma_f32_16x16x32_f16 v[52:55], a[180:183], v[172:175], v[52:55]
	v_mul_f32_e32 v16, v16, v16
	v_mul_f32_e32 v16, v16, v16
	v_rcp_f32_e32 v16, v16
	v_max_f32_e32 v17, 0, v76
	v_mfma_f32_16x16x32_f16 v[56:59], a[184:187], v[172:175], v[56:59]
	v_mul_f32_e64 v18, |v76|, v16
	v_fmamk_f32 v108, v18, 0xbf000000, v17
	v_fma_f32 v19, |v77|, v113, s48
	v_fma_f32 v19, |v77|, v19, s49
	v_mfma_f32_16x16x32_f16 v[60:63], a[188:191], v[172:175], v[60:63]
	v_fma_f32 v19, |v77|, v19, s50
	v_fma_f32 v19, |v77|, v19, s51
	v_fma_f32 v19, |v77|, v19, s52
	v_fma_f32 v19, |v77|, v19, 1.0
	v_mul_f32_e32 v19, v19, v19
	v_mfma_f32_16x16x32_f16 v[48:51], a[192:195], v[176:179], v[48:51]
	v_mul_f32_e32 v19, v19, v19
	v_mul_f32_e32 v19, v19, v19
	v_mul_f32_e32 v19, v19, v19
	v_rcp_f32_e32 v19, v19
	v_mfma_f32_16x16x32_f16 v[52:55], a[196:199], v[176:179], v[52:55]
	v_max_f32_e32 v20, 0, v77
	v_mul_f32_e64 v21, |v77|, v19
	v_fmamk_f32 v109, v21, 0xbf000000, v20
	v_fma_f32 v22, |v78|, v113, s48
	v_mfma_f32_16x16x32_f16 v[56:59], a[200:203], v[176:179], v[56:59]
	v_fma_f32 v22, |v78|, v22, s49
	v_fma_f32 v22, |v78|, v22, s50
	v_fma_f32 v22, |v78|, v22, s51
	v_fma_f32 v22, |v78|, v22, s52
	v_mfma_f32_16x16x32_f16 v[60:63], a[204:207], v[176:179], v[60:63]
	v_fma_f32 v22, |v78|, v22, 1.0
	v_mul_f32_e32 v22, v22, v22
	v_mul_f32_e32 v22, v22, v22
	v_mul_f32_e32 v22, v22, v22
	v_mfma_f32_16x16x32_f16 v[48:51], a[208:211], v[180:183], v[48:51]
	v_mul_f32_e32 v22, v22, v22
	v_rcp_f32_e32 v22, v22
	v_max_f32_e32 v23, 0, v78
	v_mul_f32_e64 v24, |v78|, v22
	v_mfma_f32_16x16x32_f16 v[52:55], a[212:215], v[180:183], v[52:55]
	v_fmamk_f32 v110, v24, 0xbf000000, v23
	v_fma_f32 v25, |v79|, v113, s48
	v_fma_f32 v25, |v79|, v25, s49
	v_fma_f32 v25, |v79|, v25, s50
	v_fma_f32 v25, |v79|, v25, s51
	v_mfma_f32_16x16x32_f16 v[56:59], a[216:219], v[180:183], v[56:59]
	v_fma_f32 v25, |v79|, v25, s52
	v_fma_f32 v25, |v79|, v25, 1.0
	v_mul_f32_e32 v25, v25, v25
	v_mul_f32_e32 v25, v25, v25
	v_mfma_f32_16x16x32_f16 v[60:63], a[220:223], v[180:183], v[60:63]
	v_mul_f32_e32 v25, v25, v25
	v_mul_f32_e32 v25, v25, v25
	v_rcp_f32_e32 v25, v25
	v_max_f32_e32 v26, 0, v79
	v_mfma_f32_16x16x32_f16 v[48:51], a[224:227], v[184:187], v[48:51]
	global_load_lds_dwordx4 v10, s[26:27] offset:1024
	v_mul_f32_e64 v27, |v79|, v25
	v_fmamk_f32 v111, v27, 0xbf000000, v26
	v_cvt_pk_f16_f32 v96, v96, v97
	v_cvt_pk_f16_f32 v97, v98, v99
	v_mfma_f32_16x16x32_f16 v[52:55], a[228:231], v[184:187], v[52:55]
	s_add_u32 s26, s26, 0x800
	s_addc_u32 s27, s27, 0
	v_cvt_pk_f16_f32 v98, v100, v101
	v_cvt_pk_f16_f32 v99, v102, v103
	v_cvt_pk_f16_f32 v100, v104, v105
	v_cvt_pk_f16_f32 v101, v106, v107
	v_mfma_f32_16x16x32_f16 v[56:59], a[232:235], v[184:187], v[56:59]
	v_cvt_pk_f16_f32 v102, v108, v109
	v_cvt_pk_f16_f32 v103, v110, v111
	global_store_dwordx4 v14, v[96:99], s[30:31]
	global_store_dwordx4 v14, v[100:103], s[30:31] offset:16
	v_mfma_f32_16x16x32_f16 v[60:63], a[236:239], v[184:187], v[60:63]
	s_add_u32 s30, s30, 0x800
	s_addc_u32 s31, s31, 0
	v_mfma_f32_16x16x32_f16 v[48:51], a[240:243], v[188:191], v[48:51]
	v_mfma_f32_16x16x32_f16 v[52:55], a[244:247], v[188:191], v[52:55]
	v_mfma_f32_16x16x32_f16 v[56:59], a[248:251], v[188:191], v[56:59]
	v_mfma_f32_16x16x32_f16 v[60:63], a[252:255], v[188:191], v[60:63]
	s_sub_u32 s24, s24, 1
	s_cmp_le_u32 s24, 1
	s_cbranch_scc0 Lg1_loop
	s_nop 7
	s_nop 7
	v_fma_f32 v16, |v48|, v113, s48
	v_fma_f32 v16, |v48|, v16, s49
	v_fma_f32 v16, |v48|, v16, s50
	v_fma_f32 v16, |v48|, v16, s51
	v_fma_f32 v16, |v48|, v16, s52
	v_fma_f32 v16, |v48|, v16, 1.0
	v_mul_f32_e32 v16, v16, v16
	v_mul_f32_e32 v16, v16, v16
	v_mul_f32_e32 v16, v16, v16
	v_mul_f32_e32 v16, v16, v16
	v_rcp_f32_e32 v16, v16
	v_max_f32_e32 v17, 0, v48
	v_mul_f32_e64 v18, |v48|, v16
	v_fmamk_f32 v96, v18, 0xbf000000, v17
	v_fma_f32 v19, |v49|, v113, s48
	v_fma_f32 v19, |v49|, v19, s49
	v_fma_f32 v19, |v49|, v19, s50
	v_fma_f32 v19, |v49|, v19, s51
	v_fma_f32 v19, |v49|, v19, s52
	v_fma_f32 v19, |v49|, v19, 1.0
	v_mul_f32_e32 v19, v19, v19
	v_mul_f32_e32 v19, v19, v19
	v_mul_f32_e32 v19, v19, v19
	v_mul_f32_e32 v19, v19, v19
	v_rcp_f32_e32 v19, v19
	v_max_f32_e32 v20, 0, v49
	v_mul_f32_e64 v21, |v49|, v19
	v_fmamk_f32 v97, v21, 0xbf000000, v20
	v_fma_f32 v22, |v50|, v113, s48
	v_fma_f32 v22, |v50|, v22, s49
	v_fma_f32 v22, |v50|, v22, s50
	v_fma_f32 v22, |v50|, v22, s51
	v_fma_f32 v22, |v50|, v22, s52
	v_fma_f32 v22, |v50|, v22, 1.0
	v_mul_f32_e32 v22, v22, v22
	v_mul_f32_e32 v22, v22, v22
	v_mul_f32_e32 v22, v22, v22
	v_mul_f32_e32 v22, v22, v22
	v_rcp_f32_e32 v22, v22
	v_max_f32_e32 v23, 0, v50
	v_mul_f32_e64 v24, |v50|, v22
	v_fmamk_f32 v98, v24, 0xbf000000, v23
	v_fma_f32 v25, |v51|, v113, s48
	v_fma_f32 v25, |v51|, v25, s49
	v_fma_f32 v25, |v51|, v25, s50
	v_fma_f32 v25, |v51|, v25, s51
	v_fma_f32 v25, |v51|, v25, s52
	v_fma_f32 v25, |v51|, v25, 1.0
	v_mul_f32_e32 v25, v25, v25
	v_mul_f32_e32 v25, v25, v25
	v_mul_f32_e32 v25, v25, v25
	v_mul_f32_e32 v25, v25, v25
	v_rcp_f32_e32 v25, v25
	v_max_f32_e32 v26, 0, v51
	v_mul_f32_e64 v27, |v51|, v25
	v_fmamk_f32 v99, v27, 0xbf000000, v26
	v_fma_f32 v16, |v52|, v113, s48
	v_fma_f32 v16, |v52|, v16, s49
	v_fma_f32 v16, |v52|, v16, s50
	v_fma_f32 v16, |v52|, v16, s51
	v_fma_f32 v16, |v52|, v16, s52
	v_fma_f32 v16, |v52|, v16, 1.0
	v_mul_f32_e32 v16, v16, v16
	v_mul_f32_e32 v16, v16, v16
	v_mul_f32_e32 v16, v16, v16
	v_mul_f32_e32 v16, v16, v16
	v_rcp_f32_e32 v16, v16
	v_max_f32_e32 v17, 0, v52
	v_mul_f32_e64 v18, |v52|, v16
	v_fmamk_f32 v100, v18, 0xbf000000, v17
	v_fma_f32 v19, |v53|, v113, s48
	v_fma_f32 v19, |v53|, v19, s49
	v_fma_f32 v19, |v53|, v19, s50
	v_fma_f32 v19, |v53|, v19, s51
	v_fma_f32 v19, |v53|, v19, s52
	v_fma_f32 v19, |v53|, v19, 1.0
	v_mul_f32_e32 v19, v19, v19
	v_mul_f32_e32 v19, v19, v19
	v_mul_f32_e32 v19, v19, v19
	v_mul_f32_e32 v19, v19, v19
	v_rcp_f32_e32 v19, v19
	v_max_f32_e32 v20, 0, v53
	v_mul_f32_e64 v21, |v53|, v19
	v_fmamk_f32 v101, v21, 0xbf000000, v20
	v_fma_f32 v22, |v54|, v113, s48
	v_fma_f32 v22, |v54|, v22, s49
	v_fma_f32 v22, |v54|, v22, s50
	v_fma_f32 v22, |v54|, v22, s51
	v_fma_f32 v22, |v54|, v22, s52
	v_fma_f32 v22, |v54|, v22, 1.0
	v_mul_f32_e32 v22, v22, v22
	v_mul_f32_e32 v22, v22, v22
	v_mul_f32_e32 v22, v22, v22
	v_mul_f32_e32 v22, v22, v22
	v_rcp_f32_e32 v22, v22
	v_max_f32_e32 v23, 0, v54
	v_mul_f32_e64 v24, |v54|, v22
	v_fmamk_f32 v102, v24, 0xbf000000, v23
	v_fma_f32 v25, |v55|, v113, s48
	v_fma_f32 v25, |v55|, v25, s49
	v_fma_f32 v25, |v55|, v25, s50
	v_fma_f32 v25, |v55|, v25, s51
	v_fma_f32 v25, |v55|, v25, s52
	v_fma_f32 v25, |v55|, v25, 1.0
	v_mul_f32_e32 v25, v25, v25
	v_mul_f32_e32 v25, v25, v25
	v_mul_f32_e32 v25, v25, v25
	v_mul_f32_e32 v25, v25, v25
	v_rcp_f32_e32 v25, v25
	v_max_f32_e32 v26, 0, v55
	v_mul_f32_e64 v27, |v55|, v25
	v_fmamk_f32 v103, v27, 0xbf000000, v26
	v_fma_f32 v16, |v56|, v113, s48
	v_fma_f32 v16, |v56|, v16, s49
	v_fma_f32 v16, |v56|, v16, s50
	v_fma_f32 v16, |v56|, v16, s51
	v_fma_f32 v16, |v56|, v16, s52
	v_fma_f32 v16, |v56|, v16, 1.0
	v_mul_f32_e32 v16, v16, v16
	v_mul_f32_e32 v16, v16, v16
	v_mul_f32_e32 v16, v16, v16
	v_mul_f32_e32 v16, v16, v16
	v_rcp_f32_e32 v16, v16
	v_max_f32_e32 v17, 0, v56
	v_mul_f32_e64 v18, |v56|, v16
	v_fmamk_f32 v104, v18, 0xbf000000, v17
	v_fma_f32 v19, |v57|, v113, s48
	v_fma_f32 v19, |v57|, v19, s49
	v_fma_f32 v19, |v57|, v19, s50
	v_fma_f32 v19, |v57|, v19, s51
	v_fma_f32 v19, |v57|, v19, s52
	v_fma_f32 v19, |v57|, v19, 1.0
	v_mul_f32_e32 v19, v19, v19
	v_mul_f32_e32 v19, v19, v19
	v_mul_f32_e32 v19, v19, v19
	v_mul_f32_e32 v19, v19, v19
	v_rcp_f32_e32 v19, v19
	v_max_f32_e32 v20, 0, v57
	v_mul_f32_e64 v21, |v57|, v19
	v_fmamk_f32 v105, v21, 0xbf000000, v20
	v_fma_f32 v22, |v58|, v113, s48
	v_fma_f32 v22, |v58|, v22, s49
	v_fma_f32 v22, |v58|, v22, s50
	v_fma_f32 v22, |v58|, v22, s51
	v_fma_f32 v22, |v58|, v22, s52
	v_fma_f32 v22, |v58|, v22, 1.0
	v_mul_f32_e32 v22, v22, v22
	v_mul_f32_e32 v22, v22, v22
	v_mul_f32_e32 v22, v22, v22
	v_mul_f32_e32 v22, v22, v22
	v_rcp_f32_e32 v22, v22
	v_max_f32_e32 v23, 0, v58
	v_mul_f32_e64 v24, |v58|, v22
	v_fmamk_f32 v106, v24, 0xbf000000, v23
	v_fma_f32 v25, |v59|, v113, s48
	v_fma_f32 v25, |v59|, v25, s49
	v_fma_f32 v25, |v59|, v25, s50
	v_fma_f32 v25, |v59|, v25, s51
	v_fma_f32 v25, |v59|, v25, s52
	v_fma_f32 v25, |v59|, v25, 1.0
	v_mul_f32_e32 v25, v25, v25
	v_mul_f32_e32 v25, v25, v25
	v_mul_f32_e32 v25, v25, v25
	v_mul_f32_e32 v25, v25, v25
	v_rcp_f32_e32 v25, v25
	v_max_f32_e32 v26, 0, v59
	v_mul_f32_e64 v27, |v59|, v25
	v_fmamk_f32 v107, v27, 0xbf000000, v26
	v_fma_f32 v16, |v60|, v113, s48
	v_fma_f32 v16, |v60|, v16, s49
	v_fma_f32 v16, |v60|, v16, s50
	v_fma_f32 v16, |v60|, v16, s51
	v_fma_f32 v16, |v60|, v16, s52
	v_fma_f32 v16, |v60|, v16, 1.0
	v_mul_f32_e32 v16, v16, v16
	v_mul_f32_e32 v16, v16, v16
	v_mul_f32_e32 v16, v16, v16
	v_mul_f32_e32 v16, v16, v16
	v_rcp_f32_e32 v16, v16
	v_max_f32_e32 v17, 0, v60
	v_mul_f32_e64 v18, |v60|, v16
	v_fmamk_f32 v108, v18, 0xbf000000, v17
	v_fma_f32 v19, |v61|, v113, s48
	v_fma_f32 v19, |v61|, v19, s49
	v_fma_f32 v19, |v61|, v19, s50
	v_fma_f32 v19, |v61|, v19, s51
	v_fma_f32 v19, |v61|, v19, s52
	v_fma_f32 v19, |v61|, v19, 1.0
	v_mul_f32_e32 v19, v19, v19
	v_mul_f32_e32 v19, v19, v19
	v_mul_f32_e32 v19, v19, v19
	v_mul_f32_e32 v19, v19, v19
	v_rcp_f32_e32 v19, v19
	v_max_f32_e32 v20, 0, v61
	v_mul_f32_e64 v21, |v61|, v19
	v_fmamk_f32 v109, v21, 0xbf000000, v20
	v_fma_f32 v22, |v62|, v113, s48
	v_fma_f32 v22, |v62|, v22, s49
	v_fma_f32 v22, |v62|, v22, s50
	v_fma_f32 v22, |v62|, v22, s51
	v_fma_f32 v22, |v62|, v22, s52
	v_fma_f32 v22, |v62|, v22, 1.0
	v_mul_f32_e32 v22, v22, v22
	v_mul_f32_e32 v22, v22, v22
	v_mul_f32_e32 v22, v22, v22
	v_mul_f32_e32 v22, v22, v22
	v_rcp_f32_e32 v22, v22
	v_max_f32_e32 v23, 0, v62
	v_mul_f32_e64 v24, |v62|, v22
	v_fmamk_f32 v110, v24, 0xbf000000, v23
	v_fma_f32 v25, |v63|, v113, s48
	v_fma_f32 v25, |v63|, v25, s49
	v_fma_f32 v25, |v63|, v25, s50
	v_fma_f32 v25, |v63|, v25, s51
	v_fma_f32 v25, |v63|, v25, s52
	v_fma_f32 v25, |v63|, v25, 1.0
	v_mul_f32_e32 v25, v25, v25
	v_mul_f32_e32 v25, v25, v25
	v_mul_f32_e32 v25, v25, v25
	v_mul_f32_e32 v25, v25, v25
	v_rcp_f32_e32 v25, v25
	v_max_f32_e32 v26, 0, v63
	v_mul_f32_e64 v27, |v63|, v25
	v_fmamk_f32 v111, v27, 0xbf000000, v26
	v_cvt_pk_f16_f32 v96, v96, v97
	v_cvt_pk_f16_f32 v97, v98, v99
	v_cvt_pk_f16_f32 v98, v100, v101
	v_cvt_pk_f16_f32 v99, v102, v103
	v_cvt_pk_f16_f32 v100, v104, v105
	v_cvt_pk_f16_f32 v101, v106, v107
	v_cvt_pk_f16_f32 v102, v108, v109
	v_cvt_pk_f16_f32 v103, v110, v111
	global_store_dwordx4 v14, v[96:99], s[30:31]
	global_store_dwordx4 v14, v[100:103], s[30:31] offset:16
	s_add_u32 s30, s30, 0x800
	s_addc_u32 s31, s31, 0
	s_endpgm
Lg1_exitA:
	s_nop 7
	s_nop 7
	v_fma_f32 v16, |v64|, v113, s48
	v_fma_f32 v16, |v64|, v16, s49
	v_fma_f32 v16, |v64|, v16, s50
	v_fma_f32 v16, |v64|, v16, s51
	v_fma_f32 v16, |v64|, v16, s52
	v_fma_f32 v16, |v64|, v16, 1.0
	v_mul_f32_e32 v16, v16, v16
	v_mul_f32_e32 v16, v16, v16
	v_mul_f32_e32 v16, v16, v16
	v_mul_f32_e32 v16, v16, v16
	v_rcp_f32_e32 v16, v16
	v_max_f32_e32 v17, 0, v64
	v_mul_f32_e64 v18, |v64|, v16
	v_fmamk_f32 v96, v18, 0xbf000000, v17
	v_fma_f32 v19, |v65|, v113, s48
	v_fma_f32 v19, |v65|, v19, s49
	v_fma_f32 v19, |v65|, v19, s50
	v_fma_f32 v19, |v65|, v19, s51
	v_fma_f32 v19, |v65|, v19, s52
	v_fma_f32 v19, |v65|, v19, 1.0
	v_mul_f32_e32 v19, v19, v19
	v_mul_f32_e32 v19, v19, v19
	v_mul_f32_e32 v19, v19, v19
	v_mul_f32_e32 v19, v19, v19
	v_rcp_f32_e32 v19, v19
	v_max_f32_e32 v20, 0, v65
	v_mul_f32_e64 v21, |v65|, v19
	v_fmamk_f32 v97, v21, 0xbf000000, v20
	v_fma_f32 v22, |v66|, v113, s48
	v_fma_f32 v22, |v66|, v22, s49
	v_fma_f32 v22, |v66|, v22, s50
	v_fma_f32 v22, |v66|, v22, s51
	v_fma_f32 v22, |v66|, v22, s52
	v_fma_f32 v22, |v66|, v22, 1.0
	v_mul_f32_e32 v22, v22, v22
	v_mul_f32_e32 v22, v22, v22
	v_mul_f32_e32 v22, v22, v22
	v_mul_f32_e32 v22, v22, v22
	v_rcp_f32_e32 v22, v22
	v_max_f32_e32 v23, 0, v66
	v_mul_f32_e64 v24, |v66|, v22
	v_fmamk_f32 v98, v24, 0xbf000000, v23
	v_fma_f32 v25, |v67|, v113, s48
	v_fma_f32 v25, |v67|, v25, s49
	v_fma_f32 v25, |v67|, v25, s50
	v_fma_f32 v25, |v67|, v25, s51
	v_fma_f32 v25, |v67|, v25, s52
	v_fma_f32 v25, |v67|, v25, 1.0
	v_mul_f32_e32 v25, v25, v25
	v_mul_f32_e32 v25, v25, v25
	v_mul_f32_e32 v25, v25, v25
	v_mul_f32_e32 v25, v25, v25
	v_rcp_f32_e32 v25, v25
	v_max_f32_e32 v26, 0, v67
	v_mul_f32_e64 v27, |v67|, v25
	v_fmamk_f32 v99, v27, 0xbf000000, v26
	v_fma_f32 v16, |v68|, v113, s48
	v_fma_f32 v16, |v68|, v16, s49
	v_fma_f32 v16, |v68|, v16, s50
	v_fma_f32 v16, |v68|, v16, s51
	v_fma_f32 v16, |v68|, v16, s52
	v_fma_f32 v16, |v68|, v16, 1.0
	v_mul_f32_e32 v16, v16, v16
	v_mul_f32_e32 v16, v16, v16
	v_mul_f32_e32 v16, v16, v16
	v_mul_f32_e32 v16, v16, v16
	v_rcp_f32_e32 v16, v16
	v_max_f32_e32 v17, 0, v68
	v_mul_f32_e64 v18, |v68|, v16
	v_fmamk_f32 v100, v18, 0xbf000000, v17
	v_fma_f32 v19, |v69|, v113, s48
	v_fma_f32 v19, |v69|, v19, s49
	v_fma_f32 v19, |v69|, v19, s50
	v_fma_f32 v19, |v69|, v19, s51
	v_fma_f32 v19, |v69|, v19, s52
	v_fma_f32 v19, |v69|, v19, 1.0
	v_mul_f32_e32 v19, v19, v19
	v_mul_f32_e32 v19, v19, v19
	v_mul_f32_e32 v19, v19, v19
	v_mul_f32_e32 v19, v19, v19
	v_rcp_f32_e32 v19, v19
	v_max_f32_e32 v20, 0, v69
	v_mul_f32_e64 v21, |v69|, v19
	v_fmamk_f32 v101, v21, 0xbf000000, v20
	v_fma_f32 v22, |v70|, v113, s48
	v_fma_f32 v22, |v70|, v22, s49
	v_fma_f32 v22, |v70|, v22, s50
	v_fma_f32 v22, |v70|, v22, s51
	v_fma_f32 v22, |v70|, v22, s52
	v_fma_f32 v22, |v70|, v22, 1.0
	v_mul_f32_e32 v22, v22, v22
	v_mul_f32_e32 v22, v22, v22
	v_mul_f32_e32 v22, v22, v22
	v_mul_f32_e32 v22, v22, v22
	v_rcp_f32_e32 v22, v22
	v_max_f32_e32 v23, 0, v70
	v_mul_f32_e64 v24, |v70|, v22
	v_fmamk_f32 v102, v24, 0xbf000000, v23
	v_fma_f32 v25, |v71|, v113, s48
	v_fma_f32 v25, |v71|, v25, s49
	v_fma_f32 v25, |v71|, v25, s50
	v_fma_f32 v25, |v71|, v25, s51
	v_fma_f32 v25, |v71|, v25, s52
	v_fma_f32 v25, |v71|, v25, 1.0
	v_mul_f32_e32 v25, v25, v25
	v_mul_f32_e32 v25, v25, v25
	v_mul_f32_e32 v25, v25, v25
	v_mul_f32_e32 v25, v25, v25
	v_rcp_f32_e32 v25, v25
	v_max_f32_e32 v26, 0, v71
	v_mul_f32_e64 v27, |v71|, v25
	v_fmamk_f32 v103, v27, 0xbf000000, v26
	v_fma_f32 v16, |v72|, v113, s48
	v_fma_f32 v16, |v72|, v16, s49
	v_fma_f32 v16, |v72|, v16, s50
	v_fma_f32 v16, |v72|, v16, s51
	v_fma_f32 v16, |v72|, v16, s52
	v_fma_f32 v16, |v72|, v16, 1.0
	v_mul_f32_e32 v16, v16, v16
	v_mul_f32_e32 v16, v16, v16
	v_mul_f32_e32 v16, v16, v16
	v_mul_f32_e32 v16, v16, v16
	v_rcp_f32_e32 v16, v16
	v_max_f32_e32 v17, 0, v72
	v_mul_f32_e64 v18, |v72|, v16
	v_fmamk_f32 v104, v18, 0xbf000000, v17
	v_fma_f32 v19, |v73|, v113, s48
	v_fma_f32 v19, |v73|, v19, s49
	v_fma_f32 v19, |v73|, v19, s50
	v_fma_f32 v19, |v73|, v19, s51
	v_fma_f32 v19, |v73|, v19, s52
	v_fma_f32 v19, |v73|, v19, 1.0
	v_mul_f32_e32 v19, v19, v19
	v_mul_f32_e32 v19, v19, v19
	v_mul_f32_e32 v19, v19, v19
	v_mul_f32_e32 v19, v19, v19
	v_rcp_f32_e32 v19, v19
	v_max_f32_e32 v20, 0, v73
	v_mul_f32_e64 v21, |v73|, v19
	v_fmamk_f32 v105, v21, 0xbf000000, v20
	v_fma_f32 v22, |v74|, v113, s48
	v_fma_f32 v22, |v74|, v22, s49
	v_fma_f32 v22, |v74|, v22, s50
	v_fma_f32 v22, |v74|, v22, s51
	v_fma_f32 v22, |v74|, v22, s52
	v_fma_f32 v22, |v74|, v22, 1.0
	v_mul_f32_e32 v22, v22, v22
	v_mul_f32_e32 v22, v22, v22
	v_mul_f32_e32 v22, v22, v22
	v_mul_f32_e32 v22, v22, v22
	v_rcp_f32_e32 v22, v22
	v_max_f32_e32 v23, 0, v74
	v_mul_f32_e64 v24, |v74|, v22
	v_fmamk_f32 v106, v24, 0xbf000000, v23
	v_fma_f32 v25, |v75|, v113, s48
	v_fma_f32 v25, |v75|, v25, s49
	v_fma_f32 v25, |v75|, v25, s50
	v_fma_f32 v25, |v75|, v25, s51
	v_fma_f32 v25, |v75|, v25, s52
	v_fma_f32 v25, |v75|, v25, 1.0
	v_mul_f32_e32 v25, v25, v25
	v_mul_f32_e32 v25, v25, v25
	v_mul_f32_e32 v25, v25, v25
	v_mul_f32_e32 v25, v25, v25
	v_rcp_f32_e32 v25, v25
	v_max_f32_e32 v26, 0, v75
	v_mul_f32_e64 v27, |v75|, v25
	v_fmamk_f32 v107, v27, 0xbf000000, v26
	v_fma_f32 v16, |v76|, v113, s48
	v_fma_f32 v16, |v76|, v16, s49
	v_fma_f32 v16, |v76|, v16, s50
	v_fma_f32 v16, |v76|, v16, s51
	v_fma_f32 v16, |v76|, v16, s52
	v_fma_f32 v16, |v76|, v16, 1.0
	v_mul_f32_e32 v16, v16, v16
	v_mul_f32_e32 v16, v16, v16
	v_mul_f32_e32 v16, v16, v16
	v_mul_f32_e32 v16, v16, v16
	v_rcp_f32_e32 v16, v16
	v_max_f32_e32 v17, 0, v76
	v_mul_f32_e64 v18, |v76|, v16
	v_fmamk_f32 v108, v18, 0xbf000000, v17
	v_fma_f32 v19, |v77|, v113, s48
	v_fma_f32 v19, |v77|, v19, s49
	v_fma_f32 v19, |v77|, v19, s50
	v_fma_f32 v19, |v77|, v19, s51
	v_fma_f32 v19, |v77|, v19, s52
	v_fma_f32 v19, |v77|, v19, 1.0
	v_mul_f32_e32 v19, v19, v19
	v_mul_f32_e32 v19, v19, v19
	v_mul_f32_e32 v19, v19, v19
	v_mul_f32_e32 v19, v19, v19
	v_rcp_f32_e32 v19, v19
	v_max_f32_e32 v20, 0, v77
	v_mul_f32_e64 v21, |v77|, v19
	v_fmamk_f32 v109, v21, 0xbf000000, v20
	v_fma_f32 v22, |v78|, v113, s48
	v_fma_f32 v22, |v78|, v22, s49
	v_fma_f32 v22, |v78|, v22, s50
	v_fma_f32 v22, |v78|, v22, s51
	v_fma_f32 v22, |v78|, v22, s52
	v_fma_f32 v22, |v78|, v22, 1.0
	v_mul_f32_e32 v22, v22, v22
	v_mul_f32_e32 v22, v22, v22
	v_mul_f32_e32 v22, v22, v22
	v_mul_f32_e32 v22, v22, v22
	v_rcp_f32_e32 v22, v22
	v_max_f32_e32 v23, 0, v78
	v_mul_f32_e64 v24, |v78|, v22
	v_fmamk_f32 v110, v24, 0xbf000000, v23
	v_fma_f32 v25, |v79|, v113, s48
	v_fma_f32 v25, |v79|, v25, s49
	v_fma_f32 v25, |v79|, v25, s50
	v_fma_f32 v25, |v79|, v25, s51
	v_fma_f32 v25, |v79|, v25, s52
	v_fma_f32 v25, |v79|, v25, 1.0
	v_mul_f32_e32 v25, v25, v25
	v_mul_f32_e32 v25, v25, v25
	v_mul_f32_e32 v25, v25, v25
	v_mul_f32_e32 v25, v25, v25
	v_rcp_f32_e32 v25, v25
	v_max_f32_e32 v26, 0, v79
	v_mul_f32_e64 v27, |v79|, v25
	v_fmamk_f32 v111, v27, 0xbf000000, v26
	v_cvt_pk_f16_f32 v96, v96, v97
	v_cvt_pk_f16_f32 v97, v98, v99
	v_cvt_pk_f16_f32 v98, v100, v101
	v_cvt_pk_f16_f32 v99, v102, v103
	v_cvt_pk_f16_f32 v100, v104, v105
	v_cvt_pk_f16_f32 v101, v106, v107
	v_cvt_pk_f16_f32 v102, v108, v109
	v_cvt_pk_f16_f32 v103, v110, v111
	global_store_dwordx4 v14, v[96:99], s[30:31]
	global_store_dwordx4 v14, v[100:103], s[30:31] offset:16
	s_add_u32 s30, s30, 0x800
	s_addc_u32 s31, s31, 0
	s_endpgm

	.amdhsa_kernel _Z6gemm_kILi1ELi2ELi2EEvPKDF16_S1_iiiPKfS1_PDF16_PfS4_
		.amdhsa_group_segment_fixed_size 81920
		.amdhsa_private_segment_fixed_size 0
		.amdhsa_kernarg_size 72
		.amdhsa_user_sgpr_count 2
		.amdhsa_user_sgpr_dispatch_ptr 0
		.amdhsa_user_sgpr_queue_ptr 0
		.amdhsa_user_sgpr_kernarg_segment_ptr 1
		.amdhsa_user_sgpr_dispatch_id 0
		.amdhsa_user_sgpr_kernarg_preload_length 0
		.amdhsa_user_sgpr_kernarg_preload_offset 0
		.amdhsa_user_sgpr_private_segment_size 0
		.amdhsa_uses_dynamic_stack 0
		.amdhsa_enable_private_segment 0
		.amdhsa_system_sgpr_workgroup_id_x 1
		.amdhsa_system_sgpr_workgroup_id_y 0
		.amdhsa_system_sgpr_workgroup_id_z 0
		.amdhsa_system_sgpr_workgroup_info 0
		.amdhsa_system_vgpr_workitem_id 0
		.amdhsa_next_free_vgpr 512
		.amdhsa_next_free_sgpr 56
		.amdhsa_accum_offset 256
		.amdhsa_reserve_vcc 1
		.amdhsa_float_round_mode_32 0
		.amdhsa_float_round_mode_16_64 0
		.amdhsa_float_denorm_mode_32 3
		.amdhsa_float_denorm_mode_16_64 3
		.amdhsa_dx10_clamp 1
		.amdhsa_ieee_mode 1
		.amdhsa_fp16_overflow 0
		.amdhsa_tg_split 0
		.amdhsa_exception_fp_ieee_invalid_op 0
		.amdhsa_exception_fp_denorm_src 0
		.amdhsa_exception_fp_ieee_div_zero 0
		.amdhsa_exception_fp_ieee_overflow 0
		.amdhsa_exception_fp_ieee_underflow 0
		.amdhsa_exception_fp_ieee_inexact 0
		.amdhsa_exception_int_div_zero 0
	.end_amdhsa_kernel

amdhsa.kernels:
  - .agpr_count:     0
    .args:
      - .actual_access:  read_only
        .address_space:  global
        .offset:         0
        .size:           8
        .value_kind:     global_buffer
      - .actual_access:  write_only
        .address_space:  global
        .offset:         8
        .size:           8
        .value_kind:     global_buffer
      - .actual_access:  read_only
        .address_space:  global
        .offset:         16
        .size:           8
        .value_kind:     global_buffer
      - .actual_access:  read_only
        .address_space:  global
        .offset:         24
        .size:           8
        .value_kind:     global_buffer
      - .actual_access:  read_only
        .address_space:  global
        .offset:         32
        .size:           8
        .value_kind:     global_buffer
      - .actual_access:  read_only
        .address_space:  global
        .offset:         40
        .size:           8
        .value_kind:     global_buffer
      - .actual_access:  write_only
        .address_space:  global
        .offset:         48
        .size:           8
        .value_kind:     global_buffer
      - .actual_access:  read_only
        .address_space:  global
        .offset:         56
        .size:           8
        .value_kind:     global_buffer
      - .actual_access:  read_only
        .address_space:  global
        .offset:         64
        .size:           8
        .value_kind:     global_buffer
      - .actual_access:  read_only
        .address_space:  global
        .offset:         72
        .size:           8
        .value_kind:     global_buffer
      - .actual_access:  read_only
        .address_space:  global
        .offset:         80
        .size:           8
        .value_kind:     global_buffer
      - .actual_access:  read_only
        .address_space:  global
        .offset:         88
        .size:           8
        .value_kind:     global_buffer
      - .actual_access:  write_only
        .address_space:  global
        .offset:         96
        .size:           8
        .value_kind:     global_buffer
      - .actual_access:  write_only
        .address_space:  global
        .offset:         104
        .size:           8
        .value_kind:     global_buffer
      - .actual_access:  write_only
        .address_space:  global
        .offset:         112
        .size:           8
        .value_kind:     global_buffer
    .group_segment_fixed_size: 51552
    .kernarg_segment_align: 8
    .kernarg_segment_size: 120
    .language:       OpenCL C
    .language_version:
      - 2
      - 0
    .max_flat_workgroup_size: 1024
    .name:           _Z6prep_kPKfPDF16_S0_S0_S0_S0_S1_S1_S1_PKiS3_S3_PiS4_S4_
    .private_segment_fixed_size: 0
    .sgpr_count:     106
    .sgpr_spill_count: 15
    .symbol:         _Z6prep_kPKfPDF16_S0_S0_S0_S0_S1_S1_S1_PKiS3_S3_PiS4_S4_.kd
    .uniform_work_group_size: 1
    .uses_dynamic_stack: false
    .vgpr_count:     48
    .vgpr_spill_count: 0
    .wavefront_size: 64
  - .agpr_count:     0
    .args:
      - .actual_access:  read_only
        .address_space:  global
        .offset:         0
        .size:           8
        .value_kind:     global_buffer
      - .actual_access:  read_only
        .address_space:  global
        .offset:         8
        .size:           8
        .value_kind:     global_buffer
      - .actual_access:  read_only
        .address_space:  global
        .offset:         16
        .size:           8
        .value_kind:     global_buffer
      - .actual_access:  read_only
        .address_space:  global
        .offset:         24
        .size:           8
        .value_kind:     global_buffer
      - .actual_access:  read_only
        .address_space:  global
        .offset:         32
        .size:           8
        .value_kind:     global_buffer
      - .actual_access:  read_only
        .address_space:  global
        .offset:         40
        .size:           8
        .value_kind:     global_buffer
      - .actual_access:  read_only
        .address_space:  global
        .offset:         48
        .size:           8
        .value_kind:     global_buffer
      - .actual_access:  read_only
        .address_space:  global
        .offset:         56
        .size:           8
        .value_kind:     global_buffer
      - .actual_access:  read_only
        .address_space:  global
        .offset:         64
        .size:           8
        .value_kind:     global_buffer
      - .actual_access:  write_only
        .address_space:  global
        .offset:         72
        .size:           8
        .value_kind:     global_buffer
      - .actual_access:  read_only
        .address_space:  global
        .offset:         80
        .size:           8
        .value_kind:     global_buffer
      - .actual_access:  read_only
        .address_space:  global
        .offset:         88
        .size:           8
        .value_kind:     global_buffer
      - .actual_access:  write_only
        .address_space:  global
        .offset:         96
        .size:           8
        .value_kind:     global_buffer
      - .actual_access:  write_only
        .address_space:  global
        .offset:         104
        .size:           8
        .value_kind:     global_buffer
    .group_segment_fixed_size: 16640
    .kernarg_segment_align: 8
    .kernarg_segment_size: 112
    .language:       OpenCL C
    .language_version:
      - 2
      - 0
    .max_flat_workgroup_size: 256
    .name:           _Z7agg_ln1PKDF16_S0_S0_PKiS2_S2_PKfS4_S4_PDF16_S4_S4_S5_S5_
    .private_segment_fixed_size: 0
    .sgpr_count:     45
    .sgpr_spill_count: 0
    .symbol:         _Z7agg_ln1PKDF16_S0_S0_PKiS2_S2_PKfS4_S4_PDF16_S4_S4_S5_S5_.kd
    .uniform_work_group_size: 1
    .uses_dynamic_stack: false
    .vgpr_count:     64
    .vgpr_spill_count: 0
    .wavefront_size: 64
  - .agpr_count:     0
    .args:
      - .actual_access:  read_only
        .address_space:  global
        .offset:         0
        .size:           8
        .value_kind:     global_buffer
      - .actual_access:  read_only
        .address_space:  global
        .offset:         8
        .size:           8
        .value_kind:     global_buffer
      - .actual_access:  read_only
        .address_space:  global
        .offset:         16
        .size:           8
        .value_kind:     global_buffer
      - .actual_access:  write_only
        .address_space:  global
        .offset:         24
        .size:           8
        .value_kind:     global_buffer
    .group_segment_fixed_size: 0
    .kernarg_segment_align: 8
    .kernarg_segment_size: 32
    .language:       OpenCL C
    .language_version:
      - 2
      - 0
    .max_flat_workgroup_size: 256
    .name:           _Z5ln2_kPKDF16_PKfS2_Pf
    .private_segment_fixed_size: 0
    .sgpr_count:     18
    .sgpr_spill_count: 0
    .symbol:         _Z5ln2_kPKDF16_PKfS2_Pf.kd
    .uniform_work_group_size: 1
    .uses_dynamic_stack: false
    .vgpr_count:     37
    .vgpr_spill_count: 0
    .wavefront_size: 64
  - .agpr_count:     256
    .args:
      - .address_space:  global
        .offset:         0
        .size:           8
        .value_kind:     global_buffer
      - .address_space:  global
        .offset:         8
        .size:           8
        .value_kind:     global_buffer
      - .offset:         16
        .size:           4
        .value_kind:     by_value
      - .offset:         20
        .size:           4
        .value_kind:     by_value
      - .offset:         24
        .size:           4
        .value_kind:     by_value
      - .actual_access:  read_only
        .address_space:  global
        .offset:         32
        .size:           8
        .value_kind:     global_buffer
      - .actual_access:  read_only
        .address_space:  global
        .offset:         40
        .size:           8
        .value_kind:     global_buffer
      - .actual_access:  write_only
        .address_space:  global
        .offset:         48
        .size:           8
        .value_kind:     global_buffer
      - .actual_access:  read_only
        .address_space:  global
        .offset:         56
        .size:           8
        .value_kind:     global_buffer
      - .actual_access:  write_only
        .address_space:  global
        .offset:         64
        .size:           8
        .value_kind:     global_buffer
    .group_segment_fixed_size: 81920
    .kernarg_segment_align: 8
    .kernarg_segment_size: 72
    .language:       OpenCL C
    .language_version:
      - 2
      - 0
    .max_flat_workgroup_size: 256
    .name:           _Z6gemm_kILi0ELi1ELi2EEvPKDF16_S1_iiiPKfS1_PDF16_PfS4_
    .private_segment_fixed_size: 0
    .sgpr_count:     54
    .sgpr_spill_count: 0
    .symbol:         _Z6gemm_kILi0ELi1ELi2EEvPKDF16_S1_iiiPKfS1_PDF16_PfS4_.kd
    .uniform_work_group_size: 1
    .uses_dynamic_stack: false
    .vgpr_count:     512
    .vgpr_spill_count: 0
    .wavefront_size: 64
  - .agpr_count:     256
    .args:
      - .address_space:  global
        .offset:         0
        .size:           8
        .value_kind:     global_buffer
      - .address_space:  global
        .offset:         8
        .size:           8
        .value_kind:     global_buffer
      - .offset:         16
        .size:           4
        .value_kind:     by_value
      - .offset:         20
        .size:           4
        .value_kind:     by_value
      - .offset:         24
        .size:           4
        .value_kind:     by_value
      - .actual_access:  read_only
        .address_space:  global
        .offset:         32
        .size:           8
        .value_kind:     global_buffer
      - .actual_access:  read_only
        .address_space:  global
        .offset:         40
        .size:           8
        .value_kind:     global_buffer
      - .actual_access:  write_only
        .address_space:  global
        .offset:         48
        .size:           8
        .value_kind:     global_buffer
      - .actual_access:  read_only
        .address_space:  global
        .offset:         56
        .size:           8
        .value_kind:     global_buffer
      - .actual_access:  read_only
        .address_space:  global
        .offset:         64
        .size:           8
        .value_kind:     global_buffer
    .group_segment_fixed_size: 81920
    .kernarg_segment_align: 8
    .kernarg_segment_size: 72
    .language:       OpenCL C
    .language_version:
      - 2
      - 0
    .max_flat_workgroup_size: 256
    .name:           _Z6gemm_kILi1ELi2ELi2EEvPKDF16_S1_iiiPKfS1_PDF16_PfS4_
    .private_segment_fixed_size: 0
    .sgpr_count:     62
    .sgpr_spill_count: 0
    .symbol:         _Z6gemm_kILi1ELi2ELi2EEvPKDF16_S1_iiiPKfS1_PDF16_PfS4_.kd
    .uniform_work_group_size: 1
    .uses_dynamic_stack: false
    .vgpr_count:     512
    .vgpr_spill_count: 0
    .wavefront_size: 64
  - .agpr_count:     256
    .args:
      - .address_space:  global
        .offset:         0
        .size:           8
        .value_kind:     global_buffer
      - .address_space:  global
        .offset:         8
        .size:           8
        .value_kind:     global_buffer
      - .offset:         16
        .size:           4
        .value_kind:     by_value
      - .offset:         20
        .size:           4
        .value_kind:     by_value
      - .offset:         24
        .size:           4
        .value_kind:     by_value
      - .actual_access:  read_only
        .address_space:  global
        .offset:         32
        .size:           8
        .value_kind:     global_buffer
      - .actual_access:  read_only
        .address_space:  global
        .offset:         40
        .size:           8
        .value_kind:     global_buffer
      - .actual_access:  write_only
        .address_space:  global
        .offset:         48
        .size:           8
        .value_kind:     global_buffer
      - .actual_access:  read_only
        .address_space:  global
        .offset:         56
        .size:           8
        .value_kind:     global_buffer
      - .actual_access:  read_only
        .address_space:  global
        .offset:         64
        .size:           8
        .value_kind:     global_buffer
    .group_segment_fixed_size: 131072
    .kernarg_segment_align: 8
    .kernarg_segment_size: 72
    .language:       OpenCL C
    .language_version:
      - 2
      - 0
    .max_flat_workgroup_size: 256
    .name:           _Z6gemm_kILi2ELi3ELi2EEvPKDF16_S1_iiiPKfS1_PDF16_PfS4_
    .private_segment_fixed_size: 0
    .sgpr_count:     54
    .sgpr_spill_count: 0
    .symbol:         _Z6gemm_kILi2ELi3ELi2EEvPKDF16_S1_iiiPKfS1_PDF16_PfS4_.kd
    .uniform_work_group_size: 1
    .uses_dynamic_stack: false
    .vgpr_count:     512
    .vgpr_spill_count: 0
    .wavefront_size: 64
